# speedup vs baseline: 1.0304x; 1.0073x over previous
.LBB1_8:
	ds_read_b32 v158, v228 offset:31040
	v_add_u32_e32 v159, v230, v139
	s_nop 2
	v_exp_f32_e32 v139, v20
	v_exp_f32_e32 v138, v24
	v_exp_f32_e32 v141, v28
	v_exp_f32_e32 v140, v32
	v_exp_f32_e32 v18, v18
	v_exp_f32_e32 v20, v22
	v_exp_f32_e32 v22, v26
	v_add_f32_e32 v24, 1.0, v138
	v_add_f32_e32 v26, 1.0, v141
	v_add_f32_e32 v19, 1.0, v139
	v_exp_f32_e32 v23, v30
	v_add_f32_e32 v27, 1.0, v140
	v_fmac_f32_e32 v24, v20, v24
	v_fmac_f32_e32 v26, v22, v26
	v_fmac_f32_e32 v19, v18, v19
	v_fmac_f32_e32 v27, v23, v27
	v_rcp_f32_e32 v18, v24
	v_rcp_f32_e32 v22, v27
	v_rcp_f32_e32 v19, v19
	v_rcp_f32_e32 v23, v26
	v_exp_f32_e32 v146, v21
	v_exp_f32_e32 v147, v25
	s_mov_b32 s8, 0xc038aa3b
	s_mov_b32 s4, 0x4038aa3b
	v_mov_b64_e32 v[160:161], s[8:9]
	v_exp_f32_e32 v148, v29
	v_exp_f32_e32 v149, v33
	v_pk_fma_f32 v[20:21], v[138:139], s[4:5], v[160:161] op_sel_hi:[1,0,0]
	s_nop 0
	v_pk_mul_f32 v[214:215], v[20:21], v[18:19]
	v_pk_fma_f32 v[18:19], v[140:141], s[4:5], v[160:161] op_sel_hi:[1,0,0]
	s_nop 0
	v_pk_mul_f32 v[212:213], v[18:19], v[22:23]
	v_add_u32_e32 v231, s7, v229
	ds_read_b128 v[18:21], v231 offset:36928
	ds_read_b128 v[22:25], v231 offset:36944
	ds_read_b128 v[26:29], v231 offset:36960
	ds_read_b128 v[30:33], v231 offset:36976
	s_waitcnt lgkmcnt(5)
	v_mfma_f32_32x32x16_bf16 v[2:17], v[46:49], v[142:145], v[2:17]
	ds_read_b128 v[138:141], v159 offset:16384
	v_add_f32_e32 v162, 1.0, v146
	v_exp_f32_e32 v163, v215
	v_exp_f32_e32 v164, v214
	v_exp_f32_e32 v165, v213
	v_exp_f32_e32 v166, v212
	v_add_f32_e32 v142, 1.0, v147
	v_add_f32_e32 v143, 1.0, v148
	v_add_f32_e32 v144, 1.0, v149
	v_mfma_f32_32x32x16_bf16 v[2:17], v[42:45], v[130:133], v[2:17]
	ds_read_b128 v[146:149], v159 offset:16416
	v_fmac_f32_e32 v162, v162, v163
	v_fmac_f32_e32 v142, v142, v164
	v_fmac_f32_e32 v143, v143, v165
	v_fmac_f32_e32 v144, v144, v166
	v_mfma_f32_32x32x16_bf16 v[2:17], v[38:41], v[154:157], v[2:17]
	ds_read_b128 v[150:153], v159 offset:16448
	v_rcp_f32_e32 v130, v162
	v_rcp_f32_e32 v131, v142
	v_rcp_f32_e32 v132, v143
	v_rcp_f32_e32 v133, v144
	s_waitcnt vmcnt(16)
	v_mfma_f32_32x32x16_bf16 v[2:17], v[34:37], v[134:137], v[2:17]
	ds_read_b128 v[178:181], v159 offset:16480
	v_fma_f32 v130, -v163, v130, v130
	v_fma_f32 v131, -v164, v131, v131
	v_fma_f32 v132, -v165, v132, v132
	v_fma_f32 v133, -v166, v133, v133
	v_add_u32_e32 v211, s6, v210
	v_cvt_pk_bf16_f32 v130, v130, v131
	v_cvt_pk_bf16_f32 v131, v132, v133
	ds_write_b64 v211, v[130:131]
	s_nop 3
	v_exp_f32_e32 v131, v4
	v_exp_f32_e32 v130, v8
	v_exp_f32_e32 v133, v12
	v_exp_f32_e32 v132, v16
	v_exp_f32_e32 v2, v2
	v_exp_f32_e32 v4, v6
	v_exp_f32_e32 v6, v10
	v_exp_f32_e32 v7, v14
	v_add_f32_e32 v3, 1.0, v131
	v_add_f32_e32 v8, 1.0, v130
	v_add_f32_e32 v10, 1.0, v133
	v_add_f32_e32 v11, 1.0, v132
	v_fmac_f32_e32 v3, v2, v3
	v_fmac_f32_e32 v8, v4, v8
	v_fmac_f32_e32 v10, v6, v10
	v_fmac_f32_e32 v11, v7, v11
	v_rcp_f32_e32 v3, v3
	v_rcp_f32_e32 v2, v8
	v_rcp_f32_e32 v7, v10
	v_rcp_f32_e32 v6, v11
	v_exp_f32_e32 v134, v5
	v_exp_f32_e32 v135, v9
	v_pk_fma_f32 v[4:5], v[130:131], s[4:5], v[160:161] op_sel_hi:[1,0,0]
	v_exp_f32_e32 v130, v13
	v_pk_mul_f32 v[204:205], v[4:5], v[2:3]
	v_pk_fma_f32 v[2:3], v[132:133], s[4:5], v[160:161] op_sel_hi:[1,0,0]
	v_exp_f32_e32 v131, v17
	v_pk_mul_f32 v[202:203], v[2:3], v[6:7]
	ds_read_b128 v[2:5], v231 offset:37056
	ds_read_b128 v[6:9], v231 offset:37072
	ds_read_b128 v[10:13], v231 offset:37088
	ds_read_b128 v[14:17], v231 offset:37104
	s_waitcnt lgkmcnt(8)
	v_mfma_f32_32x32x16_bf16 v[18:33], v[94:97], v[138:141], v[18:33]
	v_add_f32_e32 v132, 1.0, v134
	v_exp_f32_e32 v133, v205
	v_add_f32_e32 v134, 1.0, v135
	v_exp_f32_e32 v135, v204
	v_exp_f32_e32 v136, v203
	v_exp_f32_e32 v137, v202
	v_add_f32_e32 v130, 1.0, v130
	v_add_f32_e32 v131, 1.0, v131
	s_waitcnt lgkmcnt(7)
	v_mfma_f32_32x32x16_bf16 v[18:33], v[90:93], v[146:149], v[18:33]
	v_fmac_f32_e32 v132, v132, v133
	v_fmac_f32_e32 v134, v134, v135
	v_fmac_f32_e32 v130, v130, v136
	v_fmac_f32_e32 v131, v131, v137
	s_waitcnt lgkmcnt(6)
	v_mfma_f32_32x32x16_bf16 v[18:33], v[86:89], v[150:153], v[18:33]
	v_rcp_f32_e32 v132, v132
	v_rcp_f32_e32 v134, v134
	v_rcp_f32_e32 v130, v130
	v_rcp_f32_e32 v131, v131
	s_waitcnt lgkmcnt(5)
	v_mfma_f32_32x32x16_bf16 v[18:33], v[82:85], v[178:181], v[18:33]
	v_fma_f32 v132, -v133, v132, v132
	v_fma_f32 v133, -v135, v134, v134
	v_fma_f32 v134, -v136, v130, v130
	v_fma_f32 v131, -v137, v131, v131
	v_cvt_pk_bf16_f32 v130, v132, v133
	v_cvt_pk_bf16_f32 v131, v134, v131
	ds_write_b64 v211, v[130:131] offset:8
	s_waitcnt lgkmcnt(0)
	s_barrier
	s_mov_b64 s[12:13], -1
	s_and_b64 vcc, exec, s[2:3]
	s_cbranch_vccz .LBB1_10
	s_setprio 0
	s_mov_b64 s[12:13], 0

.LBB1_12:
	ds_read_b32 v194, v228 offset:31168
	ds_read_b128 v[174:177], v210
	v_add_u32_e32 v183, v230, v158
	ds_read_b128 v[170:173], v210 offset:1024
	v_exp_f32_e32 v131, v20
	v_exp_f32_e32 v130, v24
	v_exp_f32_e32 v133, v28
	v_exp_f32_e32 v132, v32
	ds_read_b128 v[166:169], v210 offset:2048
	v_exp_f32_e32 v18, v18
	v_exp_f32_e32 v20, v22
	v_exp_f32_e32 v22, v26
	v_exp_f32_e32 v23, v30
	v_add_f32_e32 v19, 1.0, v131
	v_add_f32_e32 v24, 1.0, v130
	v_add_f32_e32 v26, 1.0, v133
	v_add_f32_e32 v27, 1.0, v132
	ds_read_b128 v[162:165], v210 offset:3072
	v_fmac_f32_e32 v19, v18, v19
	v_fmac_f32_e32 v24, v20, v24
	v_fmac_f32_e32 v26, v22, v26
	v_fmac_f32_e32 v27, v23, v27
	ds_read_b128 v[158:161], v210 offset:4096
	v_rcp_f32_e32 v19, v19
	v_rcp_f32_e32 v18, v24
	v_rcp_f32_e32 v23, v26
	v_rcp_f32_e32 v22, v27
	ds_read_b128 v[154:157], v210 offset:5120
	v_exp_f32_e32 v186, v21
	v_exp_f32_e32 v187, v25
	ds_read_b128 v[142:145], v210 offset:6144
	s_mov_b32 s0, 0xc038aa3b
	s_mov_b32 s12, 0x4038aa3b
	v_mov_b64_e32 v[184:185], s[0:1]
	v_pk_fma_f32 v[20:21], v[130:131], s[12:13], v[184:185] op_sel_hi:[1,0,0]
	v_exp_f32_e32 v188, v29
	v_pk_mul_f32 v[200:201], v[20:21], v[18:19]
	v_pk_fma_f32 v[18:19], v[132:133], s[12:13], v[184:185] op_sel_hi:[1,0,0]
	v_exp_f32_e32 v189, v33
	v_pk_mul_f32 v[198:199], v[18:19], v[22:23]
	ds_read_b128 v[130:133], v210 offset:7168
	ds_read_b128 v[18:21], v231 offset:36928
	ds_read_b128 v[22:25], v231 offset:36944
	ds_read_b128 v[26:29], v231 offset:36960
	ds_read_b128 v[30:33], v231 offset:36976
	v_mfma_f32_32x32x16_bf16 v[2:17], v[46:49], v[138:141], v[2:17]
	ds_read_b128 v[134:137], v183 offset:16384
	v_add_f32_e32 v186, 1.0, v186
	v_exp_f32_e32 v190, v201
	v_exp_f32_e32 v191, v200
	v_exp_f32_e32 v192, v199
	v_exp_f32_e32 v193, v198
	v_add_f32_e32 v187, 1.0, v187
	v_add_f32_e32 v188, 1.0, v188
	v_add_f32_e32 v189, 1.0, v189
	v_mfma_f32_32x32x16_bf16 v[2:17], v[42:45], v[146:149], v[2:17]
	ds_read_b128 v[138:141], v183 offset:16416
	v_fmac_f32_e32 v186, v186, v190
	v_fmac_f32_e32 v187, v187, v191
	v_fmac_f32_e32 v188, v188, v192
	v_fmac_f32_e32 v189, v189, v193
	v_mfma_f32_32x32x16_bf16 v[2:17], v[38:41], v[150:153], v[2:17]
	ds_read_b128 v[146:149], v183 offset:16448
	v_rcp_f32_e32 v186, v186
	v_rcp_f32_e32 v187, v187
	v_rcp_f32_e32 v188, v188
	v_rcp_f32_e32 v189, v189
	v_mfma_f32_32x32x16_bf16 v[2:17], v[34:37], v[178:181], v[2:17]
	ds_read_b128 v[150:153], v183 offset:16480
	v_fma_f32 v183, -v190, v186, v186
	v_fma_f32 v186, -v191, v187, v187
	v_fma_f32 v187, -v192, v188, v188
	v_fma_f32 v188, -v193, v189, v189
	s_waitcnt vmcnt(15) lgkmcnt(0)
	v_mfma_f32_32x32x16_bf16 v[18:33], v[126:129], v[174:177], v[18:33]
	v_cvt_pk_bf16_f32 v178, v183, v186
	v_cvt_pk_bf16_f32 v179, v187, v188
	ds_write_b64 v211, v[178:179] offset:8192
	s_waitcnt vmcnt(14)
	v_mfma_f32_32x32x16_bf16 v[18:33], v[122:125], v[170:173], v[18:33]
	s_nop 0
	v_exp_f32_e32 v179, v4
	v_exp_f32_e32 v178, v8
	v_exp_f32_e32 v181, v12
	v_exp_f32_e32 v180, v16
	s_waitcnt vmcnt(13)
	v_mfma_f32_32x32x16_bf16 v[18:33], v[118:121], v[166:169], v[18:33]
	v_exp_f32_e32 v2, v2
	v_exp_f32_e32 v4, v6
	v_exp_f32_e32 v7, v10
	v_exp_f32_e32 v8, v14
	v_add_f32_e32 v3, 1.0, v179
	v_add_f32_e32 v6, 1.0, v178
	v_add_f32_e32 v10, 1.0, v181
	v_add_f32_e32 v11, 1.0, v180
	s_waitcnt vmcnt(12)
	v_mfma_f32_32x32x16_bf16 v[18:33], v[114:117], v[162:165], v[18:33]
	v_fmac_f32_e32 v3, v2, v3
	v_fmac_f32_e32 v6, v4, v6
	v_fmac_f32_e32 v10, v7, v10
	v_fmac_f32_e32 v11, v8, v11
	s_waitcnt vmcnt(11)
	v_mfma_f32_32x32x16_bf16 v[18:33], v[110:113], v[158:161], v[18:33]
	v_rcp_f32_e32 v3, v3
	v_rcp_f32_e32 v2, v6
	v_rcp_f32_e32 v7, v10
	v_rcp_f32_e32 v6, v11
	s_waitcnt vmcnt(10)
	v_mfma_f32_32x32x16_bf16 v[18:33], v[106:109], v[154:157], v[18:33]
	v_exp_f32_e32 v183, v5
	v_exp_f32_e32 v186, v9
	s_waitcnt vmcnt(9)
	v_mfma_f32_32x32x16_bf16 v[18:33], v[102:105], v[142:145], v[18:33]
	v_fma_f32 v4, v178, s12, v184
	v_fma_f32 v5, v179, s12, v184
	v_exp_f32_e32 v178, v13
	v_pk_mul_f32 v[206:207], v[4:5], v[2:3]
	v_pk_fma_f32 v[2:3], v[180:181], s[12:13], v[184:185] op_sel_hi:[1,0,0]
	v_exp_f32_e32 v179, v17
	v_pk_mul_f32 v[208:209], v[2:3], v[6:7]
	s_waitcnt vmcnt(8)
	v_mfma_f32_32x32x16_bf16 v[18:33], v[98:101], v[130:133], v[18:33]
	ds_read_b128 v[2:5], v231 offset:37056
	ds_read_b128 v[6:9], v231 offset:37072
	ds_read_b128 v[10:13], v231 offset:37088
	ds_read_b128 v[14:17], v231 offset:37104
	v_mfma_f32_32x32x16_bf16 v[18:33], v[94:97], v[134:137], v[18:33]
	v_add_f32_e32 v180, 1.0, v183
	v_exp_f32_e32 v181, v207
	v_add_f32_e32 v183, 1.0, v186
	v_exp_f32_e32 v184, v206
	v_exp_f32_e32 v185, v209
	v_exp_f32_e32 v186, v208
	v_add_f32_e32 v178, 1.0, v178
	v_add_f32_e32 v179, 1.0, v179
	v_mfma_f32_32x32x16_bf16 v[18:33], v[90:93], v[138:141], v[18:33]
	v_fmac_f32_e32 v180, v180, v181
	v_fmac_f32_e32 v183, v183, v184
	v_fmac_f32_e32 v178, v178, v185
	v_fmac_f32_e32 v179, v179, v186
	v_mfma_f32_32x32x16_bf16 v[18:33], v[86:89], v[146:149], v[18:33]
	v_rcp_f32_e32 v180, v180
	v_rcp_f32_e32 v183, v183
	v_rcp_f32_e32 v178, v178
	v_rcp_f32_e32 v179, v179
	v_mfma_f32_32x32x16_bf16 v[18:33], v[82:85], v[150:153], v[18:33]
	v_fma_f32 v180, -v181, v180, v180
	v_fma_f32 v181, -v184, v183, v183
	v_fma_f32 v183, -v185, v178, v178
	v_fma_f32 v179, -v186, v179, v179
	v_cvt_pk_bf16_f32 v178, v180, v181
	v_cvt_pk_bf16_f32 v179, v183, v179
	ds_write_b64 v211, v[178:179] offset:8200
	s_waitcnt lgkmcnt(0)
	s_barrier
	v_mov_b32_e32 v178, 0x7a40
	v_lshl_add_u32 v232, v182, 2, v178
	s_mov_b32 s1, -1
	s_branch .LBB1_14
.LBB1_13:
	v_mfma_f32_32x32x16_bf16 v[2:17], v[78:81], v[206:209], v[2:17]
	ds_read_b32 v194, v232 offset:384
	ds_read_b128 v[174:177], v210
	v_add_u32_e32 v195, v230, v233
	v_mfma_f32_32x32x16_bf16 v[2:17], v[74:77], v[190:193], v[2:17]
	ds_read_b128 v[170:173], v210 offset:1024
	v_exp_f32_e32 v199, v28
	v_exp_f32_e32 v198, v32
	v_exp_f32_e32 v197, v20
	v_exp_f32_e32 v196, v24
	v_mfma_f32_32x32x16_bf16 v[2:17], v[70:73], v[158:161], v[2:17]
	ds_read_b128 v[166:169], v210 offset:2048
	v_exp_f32_e32 v18, v18
	v_exp_f32_e32 v22, v22
	v_exp_f32_e32 v24, v26
	v_exp_f32_e32 v26, v30
	v_add_f32_e32 v20, 1.0, v197
	v_add_f32_e32 v28, 1.0, v196
	v_add_f32_e32 v30, 1.0, v199
	v_add_f32_e32 v32, 1.0, v198
	v_mfma_f32_32x32x16_bf16 v[2:17], v[66:69], v[142:145], v[2:17]
	ds_read_b128 v[162:165], v210 offset:3072
	v_exp_f32_e32 v19, v19
	v_exp_f32_e32 v23, v23
	v_exp_f32_e32 v27, v27
	v_exp_f32_e32 v31, v31
	v_fmac_f32_e32 v20, v18, v20
	v_fmac_f32_e32 v28, v22, v28
	v_fmac_f32_e32 v30, v24, v30
	v_fmac_f32_e32 v32, v26, v32
	v_mfma_f32_32x32x16_bf16 v[2:17], v[62:65], v[154:157], v[2:17]
	ds_read_b128 v[158:161], v210 offset:4096
	v_add_f32_e32 v22, 1.0, v19
	v_rcp_f32_e32 v19, v20
	v_rcp_f32_e32 v18, v28
	v_add_f32_e32 v20, 1.0, v23
	v_rcp_f32_e32 v191, v30
	v_rcp_f32_e32 v190, v32
	v_mfma_f32_32x32x16_bf16 v[2:17], v[58:61], v[182:185], v[2:17]
	ds_read_b128 v[154:157], v210 offset:5120
	v_exp_f32_e32 v206, v21
	v_exp_f32_e32 v207, v25
	v_add_f32_e32 v23, 1.0, v27
	v_rcp_f32_e32 v192, v20
	v_add_f32_e32 v20, 1.0, v31
	v_rcp_f32_e32 v193, v22
	v_mfma_f32_32x32x16_bf16 v[2:17], v[54:57], v[186:189], v[2:17]
	ds_read_b128 v[142:145], v210 offset:6144
	v_exp_f32_e32 v208, v29
	v_exp_f32_e32 v209, v33
	v_rcp_f32_e32 v183, v23
	v_rcp_f32_e32 v182, v20
	v_mfma_f32_32x32x16_bf16 v[2:17], v[50:53], v[134:137], v[2:17]
	v_mov_b64_e32 v[184:185], s[0:1]
	v_fma_f32 v20, v196, s12, v184
	v_fma_f32 v21, v197, s12, v184
	ds_read_b128 v[130:133], v210 offset:7168
	v_mul_f32_e64 v186, v20, v18
	v_mul_f32_e64 v187, v21, v19
	ds_read_b128 v[18:21], v231 offset:36928
	ds_read_b128 v[22:25], v231 offset:36944
	ds_read_b128 v[26:29], v231 offset:36960
	ds_read_b128 v[30:33], v231 offset:36976
	v_pk_fma_f32 v[134:135], v[198:199], s[12:13], v[184:185] op_sel_hi:[1,0,0]
	v_pk_fma_f32 v[200:201], v[192:193], v[220:221], v[186:187]
	v_pk_mul_f32 v[134:135], v[134:135], v[190:191]
	s_nop 0
	v_pk_fma_f32 v[198:199], v[182:183], v[222:223], v[134:135]
	v_mfma_f32_32x32x16_bf16 v[2:17], v[46:49], v[138:141], v[2:17]
	ds_read_b128 v[134:137], v195 offset:16384
	v_add_f32_e32 v182, 1.0, v206
	v_exp_f32_e32 v183, v201
	v_exp_f32_e32 v186, v200
	v_exp_f32_e32 v187, v199
	v_exp_f32_e32 v188, v198
	v_add_f32_e32 v189, 1.0, v207
	v_add_f32_e32 v190, 1.0, v208
	v_add_f32_e32 v191, 1.0, v209
	v_mfma_f32_32x32x16_bf16 v[2:17], v[42:45], v[146:149], v[2:17]
	ds_read_b128 v[138:141], v195 offset:16416
	v_fmac_f32_e32 v182, v182, v183
	v_fmac_f32_e32 v189, v189, v186
	v_fmac_f32_e32 v190, v190, v187
	v_fmac_f32_e32 v191, v191, v188
	v_mfma_f32_32x32x16_bf16 v[2:17], v[38:41], v[150:153], v[2:17]
	ds_read_b128 v[146:149], v195 offset:16448
	v_rcp_f32_e32 v182, v182
	v_rcp_f32_e32 v189, v189
	v_rcp_f32_e32 v190, v190
	v_rcp_f32_e32 v191, v191
	v_mfma_f32_32x32x16_bf16 v[2:17], v[34:37], v[178:181], v[2:17]
	ds_read_b128 v[150:153], v195 offset:16480
	v_fma_f32 v182, -v183, v182, v182
	v_fma_f32 v183, -v186, v189, v189
	v_fma_f32 v186, -v187, v190, v190
	v_fma_f32 v187, -v188, v191, v191
	s_waitcnt lgkmcnt(4)
	v_mfma_f32_32x32x16_bf16 v[18:33], v[126:129], v[174:177], v[18:33]
	v_cvt_pk_bf16_f32 v178, v182, v183
	v_cvt_pk_bf16_f32 v179, v186, v187
	ds_write_b64 v211, v[178:179] offset:8192
	v_mfma_f32_32x32x16_bf16 v[18:33], v[122:125], v[170:173], v[18:33]
	s_nop 1
	v_exp_f32_e32 v179, v4
	v_exp_f32_e32 v178, v8
	v_exp_f32_e32 v181, v12
	v_exp_f32_e32 v180, v16
	v_mfma_f32_32x32x16_bf16 v[18:33], v[118:121], v[166:169], v[18:33]
	v_exp_f32_e32 v2, v2
	v_exp_f32_e32 v6, v6
	v_exp_f32_e32 v10, v10
	v_exp_f32_e32 v12, v14
	v_add_f32_e32 v4, 1.0, v179
	v_add_f32_e32 v8, 1.0, v178
	v_add_f32_e32 v14, 1.0, v181
	v_add_f32_e32 v16, 1.0, v180
	v_mfma_f32_32x32x16_bf16 v[18:33], v[114:117], v[162:165], v[18:33]
	v_exp_f32_e32 v3, v3
	v_fmac_f32_e32 v4, v2, v4
	v_exp_f32_e32 v2, v7
	v_fmac_f32_e32 v8, v6, v8
	v_exp_f32_e32 v6, v11
	v_exp_f32_e32 v7, v15
	v_fmac_f32_e32 v14, v10, v14
	v_fmac_f32_e32 v16, v12, v16
	v_mfma_f32_32x32x16_bf16 v[18:33], v[110:113], v[158:161], v[18:33]
	v_add_f32_e32 v10, 1.0, v3
	v_rcp_f32_e32 v3, v4
	v_add_f32_e32 v4, 1.0, v2
	v_rcp_f32_e32 v2, v8
	v_rcp_f32_e32 v183, v14
	v_rcp_f32_e32 v182, v16
	v_mfma_f32_32x32x16_bf16 v[18:33], v[106:109], v[154:157], v[18:33]
	v_add_f32_e32 v6, 1.0, v6
	v_add_f32_e32 v7, 1.0, v7
	v_rcp_f32_e32 v187, v10
	v_rcp_f32_e32 v186, v4
	v_exp_f32_e32 v190, v5
	v_exp_f32_e32 v191, v9
	v_mfma_f32_32x32x16_bf16 v[18:33], v[102:105], v[142:145], v[18:33]
	v_rcp_f32_e32 v189, v6
	v_rcp_f32_e32 v188, v7
	v_exp_f32_e32 v192, v13
	v_exp_f32_e32 v193, v17
	v_pk_fma_f32 v[4:5], v[178:179], s[12:13], v[184:185] op_sel_hi:[1,0,0]
	v_mfma_f32_32x32x16_bf16 v[18:33], v[98:101], v[130:133], v[18:33]
	v_mul_f32_e64 v178, v4, v2
	v_mul_f32_e64 v179, v5, v3
	ds_read_b128 v[2:5], v231 offset:37056
	ds_read_b128 v[6:9], v231 offset:37072
	ds_read_b128 v[10:13], v231 offset:37088
	ds_read_b128 v[14:17], v231 offset:37104
	v_pk_fma_f32 v[206:207], v[186:187], v[216:217], v[178:179]
	v_pk_fma_f32 v[178:179], v[180:181], s[12:13], v[184:185] op_sel_hi:[1,0,0]
	s_nop 0
	v_pk_mul_f32 v[178:179], v[178:179], v[182:183]
	s_nop 0
	v_pk_fma_f32 v[208:209], v[188:189], v[218:219], v[178:179]
	s_waitcnt lgkmcnt(8)
	v_mfma_f32_32x32x16_bf16 v[18:33], v[94:97], v[134:137], v[18:33]
	v_add_f32_e32 v178, 1.0, v190
	v_exp_f32_e32 v179, v207
	v_add_f32_e32 v180, 1.0, v191
	v_exp_f32_e32 v181, v206
	v_exp_f32_e32 v182, v209
	v_exp_f32_e32 v183, v208
	v_add_f32_e32 v184, 1.0, v192
	v_add_f32_e32 v185, 1.0, v193
	s_waitcnt lgkmcnt(7)
	v_mfma_f32_32x32x16_bf16 v[18:33], v[90:93], v[138:141], v[18:33]
	v_fmac_f32_e32 v178, v178, v179
	v_fmac_f32_e32 v180, v180, v181
	v_fmac_f32_e32 v184, v184, v182
	v_fmac_f32_e32 v185, v185, v183
	s_waitcnt lgkmcnt(6)
	v_mfma_f32_32x32x16_bf16 v[18:33], v[86:89], v[146:149], v[18:33]
	v_rcp_f32_e32 v178, v178
	v_rcp_f32_e32 v180, v180
	v_rcp_f32_e32 v184, v184
	v_rcp_f32_e32 v185, v185
	s_waitcnt lgkmcnt(5)
	v_mfma_f32_32x32x16_bf16 v[18:33], v[82:85], v[150:153], v[18:33]
	v_fma_f32 v178, -v179, v178, v178
	v_fma_f32 v179, -v181, v180, v180
	v_fma_f32 v180, -v182, v184, v184
	v_fma_f32 v181, -v183, v185, v185
	v_cvt_pk_bf16_f32 v178, v178, v179
	v_cvt_pk_bf16_f32 v179, v180, v181
	ds_write_b64 v211, v[178:179] offset:8200
	s_waitcnt lgkmcnt(0)
	s_barrier
	s_add_i32 s1, s1, 2
	s_cmp_gt_u32 s1, 16
	v_add_u32_e32 v232, 0x200, v232
	s_cbranch_scc1 .LBB1_30

.LBB1_18:
	s_waitcnt vmcnt(7)
	v_mfma_f32_32x32x16_bf16 v[2:17], v[78:81], v[174:177], v[2:17]
	v_add_u32_e32 v192, v230, v194
	ds_read_b32 v216, v232
	ds_read_b128 v[194:197], v210 offset:8192
	s_waitcnt vmcnt(6)
	v_mfma_f32_32x32x16_bf16 v[2:17], v[74:77], v[170:173], v[2:17]
	ds_read_b128 v[178:181], v210 offset:9216
	v_exp_f32_e32 v187, v20
	v_exp_f32_e32 v186, v24
	v_exp_f32_e32 v189, v28
	v_exp_f32_e32 v188, v32
	s_waitcnt vmcnt(5)
	v_mfma_f32_32x32x16_bf16 v[2:17], v[70:73], v[166:169], v[2:17]
	ds_read_b128 v[170:173], v210 offset:10240
	v_exp_f32_e32 v18, v18
	v_exp_f32_e32 v22, v22
	v_exp_f32_e32 v24, v26
	v_exp_f32_e32 v26, v30
	v_add_f32_e32 v20, 1.0, v187
	v_add_f32_e32 v28, 1.0, v186
	v_add_f32_e32 v30, 1.0, v189
	v_add_f32_e32 v32, 1.0, v188
	s_waitcnt vmcnt(4)
	v_mfma_f32_32x32x16_bf16 v[2:17], v[66:69], v[162:165], v[2:17]
	ds_read_b128 v[166:169], v210 offset:11264
	v_exp_f32_e32 v19, v19
	v_exp_f32_e32 v23, v23
	v_exp_f32_e32 v27, v27
	v_exp_f32_e32 v31, v31
	v_fmac_f32_e32 v20, v18, v20
	v_fmac_f32_e32 v28, v22, v28
	v_fmac_f32_e32 v30, v24, v30
	v_fmac_f32_e32 v32, v26, v32
	s_waitcnt vmcnt(3)
	v_mfma_f32_32x32x16_bf16 v[2:17], v[62:65], v[158:161], v[2:17]
	ds_read_b128 v[162:165], v210 offset:12288
	v_add_f32_e32 v22, 1.0, v19
	v_rcp_f32_e32 v19, v20
	v_rcp_f32_e32 v18, v28
	v_rcp_f32_e32 v191, v30
	v_rcp_f32_e32 v190, v32
	v_add_f32_e32 v20, 1.0, v23
	s_waitcnt vmcnt(2)
	v_mfma_f32_32x32x16_bf16 v[2:17], v[58:61], v[154:157], v[2:17]
	ds_read_b128 v[174:177], v210 offset:13312
	v_rcp_f32_e32 v159, v22
	v_rcp_f32_e32 v158, v20
	v_exp_f32_e32 v160, v21
	v_exp_f32_e32 v161, v25
	v_add_f32_e32 v23, 1.0, v27
	v_add_f32_e32 v20, 1.0, v31
	s_waitcnt vmcnt(1)
	v_mfma_f32_32x32x16_bf16 v[2:17], v[54:57], v[142:145], v[2:17]
	ds_read_b128 v[182:185], v210 offset:14336
	v_rcp_f32_e32 v155, v23
	v_rcp_f32_e32 v154, v20
	v_exp_f32_e32 v193, v29
	v_exp_f32_e32 v217, v33
	s_waitcnt vmcnt(0)
	v_mfma_f32_32x32x16_bf16 v[2:17], v[50:53], v[130:133], v[2:17]
	v_mov_b64_e32 v[218:219], s[0:1]
	v_fma_f32 v20, v186, s12, v218
	v_fma_f32 v21, v187, s12, v218
	ds_read_b128 v[142:145], v210 offset:15360
	v_mul_f32_e64 v156, v20, v18
	v_mul_f32_e64 v157, v21, v19
	ds_read_b128 v[18:21], v231 offset:36928
	ds_read_b128 v[22:25], v231 offset:36944
	ds_read_b128 v[26:29], v231 offset:36960
	ds_read_b128 v[30:33], v231 offset:36976
	v_pk_fma_f32 v[130:131], v[188:189], s[12:13], v[218:219] op_sel_hi:[1,0,0]
	v_pk_fma_f32 v[214:215], v[158:159], v[214:215], v[156:157]
	v_pk_mul_f32 v[130:131], v[130:131], v[190:191]
	s_nop 0
	v_pk_fma_f32 v[212:213], v[154:155], v[212:213], v[130:131]
	v_mfma_f32_32x32x16_bf16 v[2:17], v[46:49], v[134:137], v[2:17]
	ds_read_b128 v[154:157], v192 offset:16384
	v_add_f32_e32 v130, 1.0, v160
	v_exp_f32_e32 v131, v215
	v_exp_f32_e32 v132, v214
	v_exp_f32_e32 v133, v213
	v_exp_f32_e32 v220, v212
	v_add_f32_e32 v134, 1.0, v161
	v_add_f32_e32 v135, 1.0, v193
	v_add_f32_e32 v136, 1.0, v217
	v_mfma_f32_32x32x16_bf16 v[2:17], v[42:45], v[138:141], v[2:17]
	ds_read_b128 v[158:161], v192 offset:16416
	v_fmac_f32_e32 v130, v130, v131
	v_fmac_f32_e32 v134, v134, v132
	v_fmac_f32_e32 v135, v135, v133
	v_fmac_f32_e32 v136, v136, v220
	v_mfma_f32_32x32x16_bf16 v[2:17], v[38:41], v[146:149], v[2:17]
	ds_read_b128 v[186:189], v192 offset:16448
	v_rcp_f32_e32 v130, v130
	v_rcp_f32_e32 v134, v134
	v_rcp_f32_e32 v135, v135
	v_rcp_f32_e32 v136, v136
	v_mfma_f32_32x32x16_bf16 v[2:17], v[34:37], v[150:153], v[2:17]
	ds_read_b128 v[190:193], v192 offset:16480
	v_fma_f32 v130, -v131, v130, v130
	v_fma_f32 v131, -v132, v134, v134
	v_fma_f32 v132, -v133, v135, v135
	v_fma_f32 v133, -v220, v136, v136
	s_waitcnt lgkmcnt(4)
	v_mfma_f32_32x32x16_bf16 v[18:33], v[126:129], v[194:197], v[18:33]
	v_cvt_pk_bf16_f32 v130, v130, v131
	v_cvt_pk_bf16_f32 v131, v132, v133
	ds_write_b64 v211, v[130:131]
	v_mfma_f32_32x32x16_bf16 v[18:33], v[122:125], v[178:181], v[18:33]
	s_nop 1
	v_exp_f32_e32 v131, v4
	v_exp_f32_e32 v130, v8
	v_exp_f32_e32 v133, v12
	v_exp_f32_e32 v132, v16
	v_mfma_f32_32x32x16_bf16 v[18:33], v[118:121], v[170:173], v[18:33]
	v_exp_f32_e32 v2, v2
	v_exp_f32_e32 v6, v6
	v_exp_f32_e32 v10, v10
	v_exp_f32_e32 v12, v14
	v_add_f32_e32 v4, 1.0, v131
	v_add_f32_e32 v8, 1.0, v130
	v_add_f32_e32 v14, 1.0, v133
	v_add_f32_e32 v16, 1.0, v132
	v_mfma_f32_32x32x16_bf16 v[18:33], v[114:117], v[166:169], v[18:33]
	v_exp_f32_e32 v3, v3
	v_fmac_f32_e32 v4, v2, v4
	v_exp_f32_e32 v2, v7
	v_fmac_f32_e32 v8, v6, v8
	v_exp_f32_e32 v6, v11
	v_exp_f32_e32 v7, v15
	v_fmac_f32_e32 v14, v10, v14
	v_fmac_f32_e32 v16, v12, v16
	v_mfma_f32_32x32x16_bf16 v[18:33], v[110:113], v[162:165], v[18:33]
	v_add_f32_e32 v10, 1.0, v3
	v_rcp_f32_e32 v3, v4
	v_add_f32_e32 v4, 1.0, v2
	v_rcp_f32_e32 v2, v8
	v_rcp_f32_e32 v135, v14
	v_rcp_f32_e32 v134, v16
	v_mfma_f32_32x32x16_bf16 v[18:33], v[106:109], v[174:177], v[18:33]
	v_add_f32_e32 v6, 1.0, v6
	v_add_f32_e32 v7, 1.0, v7
	v_rcp_f32_e32 v137, v10
	v_rcp_f32_e32 v136, v4
	v_exp_f32_e32 v140, v5
	v_exp_f32_e32 v141, v9
	v_mfma_f32_32x32x16_bf16 v[18:33], v[102:105], v[182:185], v[18:33]
	v_rcp_f32_e32 v139, v6
	v_rcp_f32_e32 v138, v7
	v_exp_f32_e32 v146, v13
	v_exp_f32_e32 v147, v17
	v_pk_fma_f32 v[4:5], v[130:131], s[12:13], v[218:219] op_sel_hi:[1,0,0]
	v_mfma_f32_32x32x16_bf16 v[18:33], v[98:101], v[142:145], v[18:33]
	v_mul_f32_e64 v130, v4, v2
	v_mul_f32_e64 v131, v5, v3
	ds_read_b128 v[2:5], v231 offset:37056
	ds_read_b128 v[6:9], v231 offset:37072
	ds_read_b128 v[10:13], v231 offset:37088
	ds_read_b128 v[14:17], v231 offset:37104
	v_pk_fma_f32 v[224:225], v[136:137], v[204:205], v[130:131]
	v_pk_fma_f32 v[130:131], v[132:133], s[12:13], v[218:219] op_sel_hi:[1,0,0]
	s_nop 0
	v_pk_mul_f32 v[130:131], v[130:131], v[134:135]
	s_nop 0
	v_pk_fma_f32 v[226:227], v[138:139], v[202:203], v[130:131]
	s_waitcnt lgkmcnt(8)
	v_mfma_f32_32x32x16_bf16 v[18:33], v[94:97], v[154:157], v[18:33]
	v_add_f32_e32 v130, 1.0, v140
	v_exp_f32_e32 v131, v225
	v_add_f32_e32 v132, 1.0, v141
	v_exp_f32_e32 v133, v224
	v_exp_f32_e32 v134, v227
	v_exp_f32_e32 v135, v226
	v_add_f32_e32 v136, 1.0, v146
	v_add_f32_e32 v137, 1.0, v147
	s_waitcnt lgkmcnt(7)
	v_mfma_f32_32x32x16_bf16 v[18:33], v[90:93], v[158:161], v[18:33]
	v_fmac_f32_e32 v130, v130, v131
	v_fmac_f32_e32 v132, v132, v133
	v_fmac_f32_e32 v136, v136, v134
	v_fmac_f32_e32 v137, v137, v135
	s_waitcnt lgkmcnt(6)
	v_mfma_f32_32x32x16_bf16 v[18:33], v[86:89], v[186:189], v[18:33]
	v_rcp_f32_e32 v130, v130
	v_rcp_f32_e32 v132, v132
	v_rcp_f32_e32 v136, v136
	v_rcp_f32_e32 v137, v137
	s_waitcnt lgkmcnt(5)
	v_mfma_f32_32x32x16_bf16 v[18:33], v[82:85], v[190:193], v[18:33]
	v_fma_f32 v130, -v131, v130, v130
	v_fma_f32 v131, -v133, v132, v132
	v_fma_f32 v132, -v134, v136, v136
	v_fma_f32 v133, -v135, v137, v137
	v_cvt_pk_bf16_f32 v130, v130, v131
	v_cvt_pk_bf16_f32 v131, v132, v133
	ds_write_b64 v211, v[130:131] offset:8
	s_waitcnt lgkmcnt(0)
	s_barrier
	s_mov_b64 s[16:17], -1
	s_and_b64 vcc, exec, s[2:3]
	s_cbranch_vccz .LBB1_20
	s_setprio 0
	s_mov_b64 s[16:17], 0

.LBB1_22:
	v_mfma_f32_32x32x16_bf16 v[2:17], v[78:81], v[194:197], v[2:17]
	ds_read_b32 v233, v232 offset:128
	ds_read_b128 v[202:205], v210
	v_add_u32_e32 v216, v230, v216
	v_mfma_f32_32x32x16_bf16 v[2:17], v[74:77], v[178:181], v[2:17]
	ds_read_b128 v[194:197], v210 offset:1024
	v_exp_f32_e32 v147, v20
	v_exp_f32_e32 v146, v24
	v_exp_f32_e32 v149, v28
	v_exp_f32_e32 v148, v32
	v_mfma_f32_32x32x16_bf16 v[2:17], v[70:73], v[170:173], v[2:17]
	ds_read_b128 v[138:141], v210 offset:2048
	v_exp_f32_e32 v18, v18
	v_exp_f32_e32 v22, v22
	v_exp_f32_e32 v24, v26
	v_exp_f32_e32 v26, v30
	v_add_f32_e32 v20, 1.0, v147
	v_add_f32_e32 v28, 1.0, v146
	v_add_f32_e32 v30, 1.0, v149
	v_add_f32_e32 v32, 1.0, v148
	v_mfma_f32_32x32x16_bf16 v[2:17], v[66:69], v[166:169], v[2:17]
	ds_read_b128 v[134:137], v210 offset:3072
	v_exp_f32_e32 v19, v19
	v_exp_f32_e32 v23, v23
	v_exp_f32_e32 v27, v27
	v_exp_f32_e32 v31, v31
	v_fmac_f32_e32 v20, v18, v20
	v_fmac_f32_e32 v28, v22, v28
	v_fmac_f32_e32 v30, v24, v30
	v_fmac_f32_e32 v32, v26, v32
	v_mfma_f32_32x32x16_bf16 v[2:17], v[62:65], v[162:165], v[2:17]
	ds_read_b128 v[166:169], v210 offset:4096
	v_add_f32_e32 v22, 1.0, v19
	v_rcp_f32_e32 v19, v20
	v_rcp_f32_e32 v18, v28
	v_rcp_f32_e32 v151, v30
	v_rcp_f32_e32 v150, v32
	v_add_f32_e32 v20, 1.0, v23
	v_mfma_f32_32x32x16_bf16 v[2:17], v[58:61], v[174:177], v[2:17]
	ds_read_b128 v[162:165], v210 offset:5120
	v_rcp_f32_e32 v153, v22
	v_rcp_f32_e32 v152, v20
	v_add_f32_e32 v23, 1.0, v27
	v_add_f32_e32 v20, 1.0, v31
	v_exp_f32_e32 v180, v21
	v_exp_f32_e32 v181, v25
	v_mfma_f32_32x32x16_bf16 v[2:17], v[54:57], v[182:185], v[2:17]
	ds_read_b128 v[170:173], v210 offset:6144
	v_rcp_f32_e32 v175, v23
	v_rcp_f32_e32 v174, v20
	v_exp_f32_e32 v176, v29
	v_exp_f32_e32 v177, v33
	v_mfma_f32_32x32x16_bf16 v[2:17], v[50:53], v[142:145], v[2:17]
	v_mov_b64_e32 v[178:179], s[0:1]
	v_fma_f32 v20, v146, s12, v178
	v_fma_f32 v21, v147, s12, v178
	ds_read_b128 v[130:133], v210 offset:7168
	v_mul_f32_e64 v146, v20, v18
	v_mul_f32_e64 v147, v21, v19
	ds_read_b128 v[18:21], v231 offset:36928
	ds_read_b128 v[22:25], v231 offset:36944
	ds_read_b128 v[26:29], v231 offset:36960
	ds_read_b128 v[30:33], v231 offset:36976
	v_pk_fma_f32 v[142:143], v[148:149], s[12:13], v[178:179] op_sel_hi:[1,0,0]
	v_pk_fma_f32 v[220:221], v[152:153], v[200:201], v[146:147]
	v_pk_mul_f32 v[142:143], v[142:143], v[150:151]
	s_nop 0
	v_pk_fma_f32 v[222:223], v[174:175], v[198:199], v[142:143]
	v_mfma_f32_32x32x16_bf16 v[2:17], v[46:49], v[154:157], v[2:17]
	ds_read_b128 v[146:149], v216 offset:16384
	v_add_f32_e32 v142, 1.0, v180
	v_exp_f32_e32 v143, v221
	v_exp_f32_e32 v144, v220
	v_exp_f32_e32 v145, v223
	v_exp_f32_e32 v180, v222
	v_add_f32_e32 v154, 1.0, v181
	v_add_f32_e32 v155, 1.0, v176
	v_add_f32_e32 v156, 1.0, v177
	v_mfma_f32_32x32x16_bf16 v[2:17], v[42:45], v[158:161], v[2:17]
	ds_read_b128 v[150:153], v216 offset:16416
	v_fmac_f32_e32 v142, v142, v143
	v_fmac_f32_e32 v154, v154, v144
	v_fmac_f32_e32 v155, v155, v145
	v_fmac_f32_e32 v156, v156, v180
	v_mfma_f32_32x32x16_bf16 v[2:17], v[38:41], v[186:189], v[2:17]
	ds_read_b128 v[174:177], v216 offset:16448
	v_rcp_f32_e32 v142, v142
	v_rcp_f32_e32 v154, v154
	v_rcp_f32_e32 v155, v155
	v_rcp_f32_e32 v156, v156
	v_mfma_f32_32x32x16_bf16 v[2:17], v[34:37], v[190:193], v[2:17]
	ds_read_b128 v[198:201], v216 offset:16480
	v_fma_f32 v142, -v143, v142, v142
	v_fma_f32 v143, -v144, v154, v154
	v_fma_f32 v144, -v145, v155, v155
	v_fma_f32 v145, -v180, v156, v156
	s_waitcnt lgkmcnt(4)
	v_mfma_f32_32x32x16_bf16 v[18:33], v[126:129], v[202:205], v[18:33]
	v_cvt_pk_bf16_f32 v142, v142, v143
	v_cvt_pk_bf16_f32 v143, v144, v145
	ds_write_b64 v211, v[142:143] offset:8192
	v_mfma_f32_32x32x16_bf16 v[18:33], v[122:125], v[194:197], v[18:33]
	s_nop 1
	v_exp_f32_e32 v143, v4
	v_exp_f32_e32 v142, v8
	v_exp_f32_e32 v145, v12
	v_exp_f32_e32 v144, v16
	v_mfma_f32_32x32x16_bf16 v[18:33], v[118:121], v[138:141], v[18:33]
	v_exp_f32_e32 v2, v2
	v_exp_f32_e32 v6, v6
	v_exp_f32_e32 v10, v10
	v_exp_f32_e32 v12, v14
	v_add_f32_e32 v4, 1.0, v143
	v_add_f32_e32 v8, 1.0, v142
	v_add_f32_e32 v14, 1.0, v145
	v_add_f32_e32 v16, 1.0, v144
	v_mfma_f32_32x32x16_bf16 v[18:33], v[114:117], v[134:137], v[18:33]
	v_exp_f32_e32 v3, v3
	v_fmac_f32_e32 v4, v2, v4
	v_exp_f32_e32 v2, v7
	v_fmac_f32_e32 v8, v6, v8
	v_exp_f32_e32 v6, v11
	v_exp_f32_e32 v7, v15
	v_fmac_f32_e32 v14, v10, v14
	v_fmac_f32_e32 v16, v12, v16
	v_mfma_f32_32x32x16_bf16 v[18:33], v[110:113], v[166:169], v[18:33]
	v_add_f32_e32 v10, 1.0, v3
	v_rcp_f32_e32 v3, v4
	v_add_f32_e32 v4, 1.0, v2
	v_rcp_f32_e32 v2, v8
	v_rcp_f32_e32 v155, v14
	v_rcp_f32_e32 v154, v16
	v_mfma_f32_32x32x16_bf16 v[18:33], v[106:109], v[162:165], v[18:33]
	v_add_f32_e32 v6, 1.0, v6
	v_add_f32_e32 v7, 1.0, v7
	v_rcp_f32_e32 v157, v10
	v_rcp_f32_e32 v156, v4
	v_exp_f32_e32 v160, v5
	v_exp_f32_e32 v161, v9
	v_mfma_f32_32x32x16_bf16 v[18:33], v[102:105], v[170:173], v[18:33]
	v_rcp_f32_e32 v159, v6
	v_rcp_f32_e32 v158, v7
	v_exp_f32_e32 v180, v13
	v_exp_f32_e32 v181, v17
	v_pk_fma_f32 v[4:5], v[142:143], s[12:13], v[178:179] op_sel_hi:[1,0,0]
	v_mfma_f32_32x32x16_bf16 v[18:33], v[98:101], v[130:133], v[18:33]
	v_mul_f32_e64 v142, v4, v2
	v_mul_f32_e64 v143, v5, v3
	ds_read_b128 v[2:5], v231 offset:37056
	ds_read_b128 v[6:9], v231 offset:37072
	ds_read_b128 v[10:13], v231 offset:37088
	ds_read_b128 v[14:17], v231 offset:37104
	v_pk_fma_f32 v[216:217], v[156:157], v[206:207], v[142:143]
	v_pk_fma_f32 v[142:143], v[144:145], s[12:13], v[178:179] op_sel_hi:[1,0,0]
	s_nop 0
	v_pk_mul_f32 v[142:143], v[142:143], v[154:155]
	s_nop 0
	v_pk_fma_f32 v[218:219], v[158:159], v[208:209], v[142:143]
	s_waitcnt lgkmcnt(8)
	v_mfma_f32_32x32x16_bf16 v[18:33], v[94:97], v[146:149], v[18:33]
	v_add_f32_e32 v142, 1.0, v160
	v_exp_f32_e32 v143, v217
	v_add_f32_e32 v144, 1.0, v161
	v_exp_f32_e32 v145, v216
	v_exp_f32_e32 v154, v219
	v_exp_f32_e32 v155, v218
	v_add_f32_e32 v156, 1.0, v180
	v_add_f32_e32 v157, 1.0, v181
	s_waitcnt lgkmcnt(7)
	v_mfma_f32_32x32x16_bf16 v[18:33], v[90:93], v[150:153], v[18:33]
	v_fmac_f32_e32 v142, v142, v143
	v_fmac_f32_e32 v144, v144, v145
	v_fmac_f32_e32 v156, v156, v154
	v_fmac_f32_e32 v157, v157, v155
	s_waitcnt lgkmcnt(6)
	v_mfma_f32_32x32x16_bf16 v[18:33], v[86:89], v[174:177], v[18:33]
	v_rcp_f32_e32 v142, v142
	v_rcp_f32_e32 v144, v144
	v_rcp_f32_e32 v156, v156
	v_rcp_f32_e32 v157, v157
	s_waitcnt lgkmcnt(5)
	v_mfma_f32_32x32x16_bf16 v[18:33], v[82:85], v[198:201], v[18:33]
	v_fma_f32 v142, -v143, v142, v142
	v_fma_f32 v143, -v145, v144, v144
	v_fma_f32 v144, -v154, v156, v156
	v_fma_f32 v145, -v155, v157, v157
	v_cvt_pk_bf16_f32 v142, v142, v143
	v_cvt_pk_bf16_f32 v143, v144, v145
	ds_write_b64 v211, v[142:143] offset:8200
	s_waitcnt lgkmcnt(0)
	s_barrier
	s_mov_b64 s[16:17], -1
	s_and_b64 vcc, exec, s[2:3]
	s_cbranch_vccz .LBB1_24
	s_setprio 0
	s_mov_b64 s[16:17], 0

.LBB1_26:
	v_mfma_f32_32x32x16_bf16 v[2:17], v[78:81], v[202:205], v[2:17]
	v_add_u32_e32 v234, v230, v233
	ds_read_b32 v233, v232 offset:256
	ds_read_b128 v[206:209], v210 offset:8192
	v_mfma_f32_32x32x16_bf16 v[2:17], v[74:77], v[194:197], v[2:17]
	ds_read_b128 v[190:193], v210 offset:9216
	v_exp_f32_e32 v179, v20
	v_exp_f32_e32 v178, v24
	v_exp_f32_e32 v181, v28
	v_exp_f32_e32 v180, v32
	v_mfma_f32_32x32x16_bf16 v[2:17], v[70:73], v[138:141], v[2:17]
	ds_read_b128 v[158:161], v210 offset:10240
	v_exp_f32_e32 v18, v18
	v_exp_f32_e32 v22, v22
	v_exp_f32_e32 v24, v26
	v_exp_f32_e32 v26, v30
	v_add_f32_e32 v20, 1.0, v179
	v_add_f32_e32 v28, 1.0, v178
	v_add_f32_e32 v30, 1.0, v181
	v_add_f32_e32 v32, 1.0, v180
	v_mfma_f32_32x32x16_bf16 v[2:17], v[66:69], v[134:137], v[2:17]
	ds_read_b128 v[142:145], v210 offset:11264
	v_exp_f32_e32 v19, v19
	v_exp_f32_e32 v23, v23
	v_exp_f32_e32 v27, v27
	v_exp_f32_e32 v31, v31
	v_fmac_f32_e32 v20, v18, v20
	v_fmac_f32_e32 v28, v22, v28
	v_fmac_f32_e32 v30, v24, v30
	v_fmac_f32_e32 v32, v26, v32
	v_mfma_f32_32x32x16_bf16 v[2:17], v[62:65], v[166:169], v[2:17]
	ds_read_b128 v[154:157], v210 offset:12288
	v_add_f32_e32 v22, 1.0, v19
	v_rcp_f32_e32 v19, v20
	v_rcp_f32_e32 v18, v28
	v_rcp_f32_e32 v139, v30
	v_rcp_f32_e32 v138, v32
	v_add_f32_e32 v20, 1.0, v23
	v_mfma_f32_32x32x16_bf16 v[2:17], v[58:61], v[162:165], v[2:17]
	ds_read_b128 v[182:185], v210 offset:13312
	v_rcp_f32_e32 v141, v22
	v_rcp_f32_e32 v140, v20
	v_add_f32_e32 v23, 1.0, v27
	v_add_f32_e32 v20, 1.0, v31
	v_exp_f32_e32 v168, v21
	v_exp_f32_e32 v169, v25
	v_mfma_f32_32x32x16_bf16 v[2:17], v[54:57], v[170:173], v[2:17]
	ds_read_b128 v[186:189], v210 offset:14336
	v_rcp_f32_e32 v163, v23
	v_rcp_f32_e32 v162, v20
	v_exp_f32_e32 v194, v29
	v_exp_f32_e32 v195, v33
	v_mfma_f32_32x32x16_bf16 v[2:17], v[50:53], v[130:133], v[2:17]
	v_mov_b64_e32 v[164:165], s[0:1]
	v_fma_f32 v20, v178, s12, v164
	v_fma_f32 v21, v179, s12, v164
	ds_read_b128 v[134:137], v210 offset:15360
	v_mul_f32_e64 v166, v20, v18
	v_mul_f32_e64 v167, v21, v19
	ds_read_b128 v[18:21], v231 offset:36928
	ds_read_b128 v[22:25], v231 offset:36944
	ds_read_b128 v[26:29], v231 offset:36960
	ds_read_b128 v[30:33], v231 offset:36976
	v_pk_fma_f32 v[130:131], v[180:181], s[12:13], v[164:165] op_sel_hi:[1,0,0]
	v_pk_fma_f32 v[214:215], v[140:141], v[214:215], v[166:167]
	v_pk_mul_f32 v[130:131], v[130:131], v[138:139]
	s_nop 0
	v_pk_fma_f32 v[212:213], v[162:163], v[212:213], v[130:131]
	v_mfma_f32_32x32x16_bf16 v[2:17], v[46:49], v[146:149], v[2:17]
	ds_read_b128 v[138:141], v234 offset:16384
	v_add_f32_e32 v130, 1.0, v168
	v_exp_f32_e32 v131, v215
	v_exp_f32_e32 v132, v214
	v_exp_f32_e32 v133, v213
	v_exp_f32_e32 v162, v212
	v_add_f32_e32 v163, 1.0, v169
	v_add_f32_e32 v166, 1.0, v194
	v_add_f32_e32 v167, 1.0, v195
	v_mfma_f32_32x32x16_bf16 v[2:17], v[42:45], v[150:153], v[2:17]
	ds_read_b128 v[146:149], v234 offset:16416
	v_fmac_f32_e32 v130, v130, v131
	v_fmac_f32_e32 v163, v163, v132
	v_fmac_f32_e32 v166, v166, v133
	v_fmac_f32_e32 v167, v167, v162
	v_mfma_f32_32x32x16_bf16 v[2:17], v[38:41], v[174:177], v[2:17]
	ds_read_b128 v[150:153], v234 offset:16448
	v_rcp_f32_e32 v130, v130
	v_rcp_f32_e32 v163, v163
	v_rcp_f32_e32 v166, v166
	v_rcp_f32_e32 v167, v167
	v_mfma_f32_32x32x16_bf16 v[2:17], v[34:37], v[198:201], v[2:17]
	ds_read_b128 v[178:181], v234 offset:16480
	v_fma_f32 v130, -v131, v130, v130
	v_fma_f32 v131, -v132, v163, v163
	v_fma_f32 v132, -v133, v166, v166
	v_fma_f32 v133, -v162, v167, v167
	s_waitcnt lgkmcnt(4)
	v_mfma_f32_32x32x16_bf16 v[18:33], v[126:129], v[206:209], v[18:33]
	v_cvt_pk_bf16_f32 v130, v130, v131
	v_cvt_pk_bf16_f32 v131, v132, v133
	ds_write_b64 v211, v[130:131]
	v_mfma_f32_32x32x16_bf16 v[18:33], v[122:125], v[190:193], v[18:33]
	s_nop 1
	v_exp_f32_e32 v131, v4
	v_exp_f32_e32 v130, v8
	v_exp_f32_e32 v133, v12
	v_exp_f32_e32 v132, v16
	v_mfma_f32_32x32x16_bf16 v[18:33], v[118:121], v[158:161], v[18:33]
	v_exp_f32_e32 v2, v2
	v_exp_f32_e32 v6, v6
	v_exp_f32_e32 v10, v10
	v_exp_f32_e32 v12, v14
	v_add_f32_e32 v4, 1.0, v131
	v_add_f32_e32 v8, 1.0, v130
	v_add_f32_e32 v14, 1.0, v133
	v_add_f32_e32 v16, 1.0, v132
	v_mfma_f32_32x32x16_bf16 v[18:33], v[114:117], v[142:145], v[18:33]
	v_exp_f32_e32 v3, v3
	v_fmac_f32_e32 v4, v2, v4
	v_exp_f32_e32 v2, v7
	v_fmac_f32_e32 v8, v6, v8
	v_exp_f32_e32 v6, v11
	v_exp_f32_e32 v7, v15
	v_fmac_f32_e32 v14, v10, v14
	v_fmac_f32_e32 v16, v12, v16
	v_mfma_f32_32x32x16_bf16 v[18:33], v[110:113], v[154:157], v[18:33]
	v_add_f32_e32 v10, 1.0, v3
	v_rcp_f32_e32 v3, v4
	v_add_f32_e32 v4, 1.0, v2
	v_rcp_f32_e32 v2, v8
	v_rcp_f32_e32 v163, v14
	v_rcp_f32_e32 v162, v16
	v_mfma_f32_32x32x16_bf16 v[18:33], v[106:109], v[182:185], v[18:33]
	v_add_f32_e32 v6, 1.0, v6
	v_add_f32_e32 v7, 1.0, v7
	v_rcp_f32_e32 v167, v10
	v_rcp_f32_e32 v166, v4
	v_exp_f32_e32 v170, v5
	v_exp_f32_e32 v171, v9
	v_mfma_f32_32x32x16_bf16 v[18:33], v[102:105], v[186:189], v[18:33]
	v_rcp_f32_e32 v169, v6
	v_rcp_f32_e32 v168, v7
	v_exp_f32_e32 v172, v13
	v_exp_f32_e32 v173, v17
	v_pk_fma_f32 v[4:5], v[130:131], s[12:13], v[164:165] op_sel_hi:[1,0,0]
	v_mfma_f32_32x32x16_bf16 v[18:33], v[98:101], v[134:137], v[18:33]
	v_mul_f32_e64 v130, v4, v2
	v_mul_f32_e64 v131, v5, v3
	ds_read_b128 v[2:5], v231 offset:37056
	ds_read_b128 v[6:9], v231 offset:37072
	ds_read_b128 v[10:13], v231 offset:37088
	ds_read_b128 v[14:17], v231 offset:37104
	v_pk_fma_f32 v[204:205], v[166:167], v[224:225], v[130:131]
	v_pk_fma_f32 v[130:131], v[132:133], s[12:13], v[164:165] op_sel_hi:[1,0,0]
	s_nop 0
	v_pk_mul_f32 v[130:131], v[130:131], v[162:163]
	s_nop 0
	v_pk_fma_f32 v[202:203], v[168:169], v[226:227], v[130:131]
	s_waitcnt lgkmcnt(8)
	v_mfma_f32_32x32x16_bf16 v[18:33], v[94:97], v[138:141], v[18:33]
	v_add_f32_e32 v130, 1.0, v170
	v_exp_f32_e32 v131, v205
	v_add_f32_e32 v132, 1.0, v171
	v_exp_f32_e32 v133, v204
	v_exp_f32_e32 v162, v203
	v_exp_f32_e32 v163, v202
	v_add_f32_e32 v164, 1.0, v172
	v_add_f32_e32 v165, 1.0, v173
	s_waitcnt lgkmcnt(7)
	v_mfma_f32_32x32x16_bf16 v[18:33], v[90:93], v[146:149], v[18:33]
	v_fmac_f32_e32 v130, v130, v131
	v_fmac_f32_e32 v132, v132, v133
	v_fmac_f32_e32 v164, v164, v162
	v_fmac_f32_e32 v165, v165, v163
	s_waitcnt lgkmcnt(6)
	v_mfma_f32_32x32x16_bf16 v[18:33], v[86:89], v[150:153], v[18:33]
	v_rcp_f32_e32 v130, v130
	v_rcp_f32_e32 v132, v132
	v_rcp_f32_e32 v164, v164
	v_rcp_f32_e32 v165, v165
	s_waitcnt lgkmcnt(5)
	v_mfma_f32_32x32x16_bf16 v[18:33], v[82:85], v[178:181], v[18:33]
	v_fma_f32 v130, -v131, v130, v130
	v_fma_f32 v131, -v133, v132, v132
	v_fma_f32 v132, -v162, v164, v164
	v_fma_f32 v133, -v163, v165, v165
	v_cvt_pk_bf16_f32 v130, v130, v131
	v_cvt_pk_bf16_f32 v131, v132, v133
	ds_write_b64 v211, v[130:131] offset:8
	s_waitcnt lgkmcnt(0)
	s_barrier
	s_mov_b64 s[16:17], -1
	s_and_b64 vcc, exec, s[2:3]
	s_cbranch_vccz .LBB1_28
	s_setprio 0
	s_mov_b64 s[16:17], 0

.LBB1_34:
	v_mfma_f32_32x32x16_bf16 v[2:17], v[78:81], v[174:177], v[2:17]
	ds_read_b128 v[178:181], v210 offset:8192
	v_add_u32_e32 v182, v230, v194
	v_mfma_f32_32x32x16_bf16 v[2:17], v[74:77], v[170:173], v[2:17]
	ds_read_b128 v[174:177], v210 offset:9216
	v_exp_f32_e32 v20, v20
	v_exp_f32_e32 v24, v24
	v_exp_f32_e32 v28, v28
	v_exp_f32_e32 v32, v32
	v_mfma_f32_32x32x16_bf16 v[2:17], v[70:73], v[166:169], v[2:17]
	ds_read_b128 v[170:173], v210 offset:10240
	v_exp_f32_e32 v18, v18
	v_exp_f32_e32 v22, v22
	v_exp_f32_e32 v26, v26
	v_exp_f32_e32 v30, v30
	v_add_f32_e32 v183, 1.0, v20
	v_add_f32_e32 v184, 1.0, v24
	v_add_f32_e32 v185, 1.0, v28
	v_add_f32_e32 v186, 1.0, v32
	v_mfma_f32_32x32x16_bf16 v[2:17], v[66:69], v[162:165], v[2:17]
	ds_read_b128 v[166:169], v210 offset:11264
	v_exp_f32_e32 v19, v19
	v_fmac_f32_e32 v183, v18, v183
	v_exp_f32_e32 v18, v23
	v_exp_f32_e32 v23, v27
	v_exp_f32_e32 v27, v31
	v_fmac_f32_e32 v184, v22, v184
	v_fmac_f32_e32 v185, v26, v185
	v_fmac_f32_e32 v186, v30, v186
	v_mfma_f32_32x32x16_bf16 v[2:17], v[62:65], v[158:161], v[2:17]
	ds_read_b128 v[162:165], v210 offset:12288
	v_rcp_f32_e32 v22, v183
	v_rcp_f32_e32 v26, v184
	v_rcp_f32_e32 v30, v185
	v_rcp_f32_e32 v31, v186
	v_mov_b32_e32 v183, 0xc038aa3b
	v_add_f32_e32 v19, 1.0, v19
	v_fmamk_f32 v20, v20, 0x4038aa3b, v183
	v_add_f32_e32 v18, 1.0, v18
	v_fmamk_f32 v24, v24, 0x4038aa3b, v183
	v_mfma_f32_32x32x16_bf16 v[2:17], v[58:61], v[154:157], v[2:17]
	ds_read_b128 v[158:161], v210 offset:13312
	v_rcp_f32_e32 v19, v19
	v_add_f32_e32 v23, 1.0, v23
	v_rcp_f32_e32 v184, v18
	v_exp_f32_e32 v185, v21
	v_exp_f32_e32 v186, v25
	v_fmamk_f32 v18, v28, 0x4038aa3b, v183
	v_add_f32_e32 v21, 1.0, v27
	v_fmamk_f32 v25, v32, 0x4038aa3b, v183
	v_mfma_f32_32x32x16_bf16 v[2:17], v[54:57], v[142:145], v[2:17]
	ds_read_b128 v[154:157], v210 offset:14336
	v_mul_f32_e32 v187, v20, v22
	v_rcp_f32_e32 v188, v23
	v_rcp_f32_e32 v189, v21
	v_exp_f32_e32 v190, v29
	v_exp_f32_e32 v191, v33
	v_mul_f32_e32 v192, v24, v26
	v_mul_f32_e32 v193, v18, v30
	v_mul_f32_e32 v194, v25, v31
	v_mfma_f32_32x32x16_bf16 v[2:17], v[50:53], v[130:133], v[2:17]
	ds_read_b128 v[142:145], v210 offset:15360
	v_fmac_f32_e32 v187, v19, v215
	ds_read_b128 v[18:21], v231 offset:36928
	ds_read_b128 v[22:25], v231 offset:36944
	ds_read_b128 v[26:29], v231 offset:36960
	ds_read_b128 v[30:33], v231 offset:36976
	v_fmac_f32_e32 v192, v184, v214
	v_fmac_f32_e32 v193, v188, v213
	v_fmac_f32_e32 v194, v189, v212
	v_mfma_f32_32x32x16_bf16 v[2:17], v[46:49], v[134:137], v[2:17]
	ds_read_b128 v[130:133], v182 offset:16384
	v_add_f32_e32 v184, 1.0, v185
	v_exp_f32_e32 v185, v187
	v_exp_f32_e32 v187, v192
	v_exp_f32_e32 v188, v193
	v_exp_f32_e32 v189, v194
	v_add_f32_e32 v186, 1.0, v186
	v_add_f32_e32 v190, 1.0, v190
	v_add_f32_e32 v191, 1.0, v191
	v_mfma_f32_32x32x16_bf16 v[2:17], v[42:45], v[138:141], v[2:17]
	ds_read_b128 v[134:137], v182 offset:16416
	v_fmac_f32_e32 v184, v184, v185
	v_fmac_f32_e32 v186, v186, v187
	v_fmac_f32_e32 v190, v190, v188
	v_fmac_f32_e32 v191, v191, v189
	v_mfma_f32_32x32x16_bf16 v[2:17], v[38:41], v[146:149], v[2:17]
	ds_read_b128 v[138:141], v182 offset:16448
	v_rcp_f32_e32 v184, v184
	v_rcp_f32_e32 v186, v186
	v_rcp_f32_e32 v190, v190
	v_rcp_f32_e32 v191, v191
	v_mfma_f32_32x32x16_bf16 v[2:17], v[34:37], v[150:153], v[2:17]
	ds_read_b128 v[146:149], v182 offset:16480
	v_fma_f32 v182, -v185, v184, v184
	v_fma_f32 v184, -v187, v186, v186
	v_fma_f32 v185, -v188, v190, v190
	v_fma_f32 v186, -v189, v191, v191
	s_waitcnt lgkmcnt(4)
	v_mfma_f32_32x32x16_bf16 v[18:33], v[126:129], v[178:181], v[18:33]
	v_cvt_pk_bf16_f32 v150, v182, v184
	v_cvt_pk_bf16_f32 v151, v185, v186
	ds_write_b64 v211, v[150:151]
	v_mfma_f32_32x32x16_bf16 v[18:33], v[122:125], v[174:177], v[18:33]
	s_nop 1
	v_exp_f32_e32 v4, v4
	v_exp_f32_e32 v8, v8
	v_exp_f32_e32 v12, v12
	v_exp_f32_e32 v16, v16
	v_mfma_f32_32x32x16_bf16 v[18:33], v[118:121], v[170:173], v[18:33]
	v_exp_f32_e32 v2, v2
	v_exp_f32_e32 v6, v6
	v_exp_f32_e32 v10, v10
	v_exp_f32_e32 v14, v14
	v_add_f32_e32 v122, 1.0, v4
	v_add_f32_e32 v123, 1.0, v8
	v_add_f32_e32 v118, 1.0, v12
	v_add_f32_e32 v119, 1.0, v16
	v_mfma_f32_32x32x16_bf16 v[18:33], v[114:117], v[166:169], v[18:33]
	v_exp_f32_e32 v3, v3
	v_fmac_f32_e32 v122, v2, v122
	v_exp_f32_e32 v2, v7
	v_fmac_f32_e32 v123, v6, v123
	v_exp_f32_e32 v6, v11
	v_exp_f32_e32 v7, v15
	v_fmac_f32_e32 v118, v10, v118
	v_fmac_f32_e32 v119, v14, v119
	v_mfma_f32_32x32x16_bf16 v[18:33], v[110:113], v[162:165], v[18:33]
	v_rcp_f32_e32 v10, v122
	v_rcp_f32_e32 v11, v123
	v_rcp_f32_e32 v14, v118
	v_rcp_f32_e32 v15, v119
	v_add_f32_e32 v3, 1.0, v3
	v_fmamk_f32 v4, v4, 0x4038aa3b, v183
	v_add_f32_e32 v2, 1.0, v2
	v_fmamk_f32 v8, v8, 0x4038aa3b, v183
	v_mfma_f32_32x32x16_bf16 v[18:33], v[106:109], v[158:161], v[18:33]
	v_rcp_f32_e32 v3, v3
	v_rcp_f32_e32 v2, v2
	v_add_f32_e32 v6, 1.0, v6
	v_fmamk_f32 v12, v12, 0x4038aa3b, v183
	v_exp_f32_e32 v110, v5
	v_add_f32_e32 v5, 1.0, v7
	v_exp_f32_e32 v111, v9
	v_fmac_f32_e32 v183, 0x4038aa3b, v16
	v_mfma_f32_32x32x16_bf16 v[18:33], v[102:105], v[154:157], v[18:33]
	v_mul_f32_e32 v106, v4, v10
	v_mul_f32_e32 v107, v8, v11
	v_rcp_f32_e32 v108, v6
	v_rcp_f32_e32 v109, v5
	v_exp_f32_e32 v112, v13
	v_exp_f32_e32 v113, v17
	v_mul_f32_e32 v102, v12, v14
	v_mul_f32_e32 v103, v183, v15
	v_mfma_f32_32x32x16_bf16 v[18:33], v[98:101], v[142:145], v[18:33]
	v_fmac_f32_e32 v106, v3, v205
	v_fmac_f32_e32 v107, v2, v204
	ds_read_b128 v[2:5], v231 offset:37056
	ds_read_b128 v[6:9], v231 offset:37072
	ds_read_b128 v[10:13], v231 offset:37088
	ds_read_b128 v[14:17], v231 offset:37104
	v_fmac_f32_e32 v102, v108, v203
	v_fmac_f32_e32 v103, v109, v202
	s_waitcnt lgkmcnt(8)
	v_mfma_f32_32x32x16_bf16 v[18:33], v[94:97], v[130:133], v[18:33]
	v_add_f32_e32 v98, 1.0, v110
	v_exp_f32_e32 v99, v106
	v_add_f32_e32 v100, 1.0, v111
	v_exp_f32_e32 v101, v107
	v_exp_f32_e32 v102, v102
	v_exp_f32_e32 v103, v103
	v_add_f32_e32 v94, 1.0, v112
	v_add_f32_e32 v95, 1.0, v113
	s_waitcnt lgkmcnt(7)
	v_mfma_f32_32x32x16_bf16 v[18:33], v[90:93], v[134:137], v[18:33]
	v_fmac_f32_e32 v98, v98, v99
	v_fmac_f32_e32 v100, v100, v101
	v_fmac_f32_e32 v94, v94, v102
	v_fmac_f32_e32 v95, v95, v103
	s_waitcnt lgkmcnt(6)
	v_mfma_f32_32x32x16_bf16 v[18:33], v[86:89], v[138:141], v[18:33]
	v_rcp_f32_e32 v90, v98
	v_rcp_f32_e32 v91, v100
	v_rcp_f32_e32 v92, v94
	v_rcp_f32_e32 v93, v95
	s_waitcnt lgkmcnt(5)
	v_mfma_f32_32x32x16_bf16 v[18:33], v[82:85], v[146:149], v[18:33]
	v_fma_f32 v86, -v99, v90, v90
	v_fma_f32 v87, -v101, v91, v91
	v_fma_f32 v88, -v102, v92, v92
	v_fma_f32 v89, -v103, v93, v93
	v_cvt_pk_bf16_f32 v82, v86, v87
	v_cvt_pk_bf16_f32 v83, v88, v89
	ds_write_b64 v211, v[82:83] offset:8
	s_waitcnt lgkmcnt(0)
	s_barrier
	s_mov_b64 s[0:1], -1
	s_and_b64 vcc, exec, s[2:3]
	s_cbranch_vccz .LBB1_36
	s_setprio 0
	s_mov_b64 s[0:1], 0

.LBB1_38:
	v_mfma_f32_32x32x16_bf16 v[2:17], v[78:81], v[178:181], v[2:17]
	v_exp_f32_e32 v20, v20
	v_exp_f32_e32 v24, v24
	v_exp_f32_e32 v28, v28
	v_exp_f32_e32 v32, v32
	v_mfma_f32_32x32x16_bf16 v[2:17], v[74:77], v[174:177], v[2:17]
	v_exp_f32_e32 v18, v18
	v_add_f32_e32 v74, 1.0, v20
	v_exp_f32_e32 v22, v22
	v_add_f32_e32 v75, 1.0, v24
	v_exp_f32_e32 v26, v26
	v_exp_f32_e32 v30, v30
	v_mfma_f32_32x32x16_bf16 v[2:17], v[70:73], v[170:173], v[2:17]
	v_add_f32_e32 v70, 1.0, v28
	v_add_f32_e32 v71, 1.0, v32
	v_exp_f32_e32 v19, v19
	v_fmac_f32_e32 v74, v18, v74
	v_exp_f32_e32 v18, v23
	v_fmac_f32_e32 v75, v22, v75
	v_exp_f32_e32 v22, v27
	v_exp_f32_e32 v23, v31
	v_mfma_f32_32x32x16_bf16 v[2:17], v[66:69], v[166:169], v[2:17]
	v_fmac_f32_e32 v70, v26, v70
	v_fmac_f32_e32 v71, v30, v71
	v_mov_b32_e32 v27, 0xc038aa3b
	v_add_f32_e32 v19, 1.0, v19
	v_rcp_f32_e32 v26, v74
	v_rcp_f32_e32 v30, v75
	v_rcp_f32_e32 v31, v70
	v_rcp_f32_e32 v66, v71
	v_mfma_f32_32x32x16_bf16 v[2:17], v[62:65], v[162:165], v[2:17]
	v_fmamk_f32 v20, v20, 0x4038aa3b, v27
	v_add_f32_e32 v18, 1.0, v18
	v_fmamk_f32 v24, v24, 0x4038aa3b, v27
	v_add_f32_e32 v22, 1.0, v22
	v_fmamk_f32 v28, v28, 0x4038aa3b, v27
	v_rcp_f32_e32 v19, v19
	v_rcp_f32_e32 v18, v18
	v_exp_f32_e32 v21, v21
	v_exp_f32_e32 v25, v25
	v_mfma_f32_32x32x16_bf16 v[2:17], v[58:61], v[158:161], v[2:17]
	v_add_f32_e32 v23, 1.0, v23
	v_fmamk_f32 v32, v32, 0x4038aa3b, v27
	v_mul_f32_e32 v20, v20, v26
	v_mul_f32_e32 v24, v24, v30
	v_rcp_f32_e32 v22, v22
	v_rcp_f32_e32 v23, v23
	v_exp_f32_e32 v26, v29
	v_exp_f32_e32 v29, v33
	v_mfma_f32_32x32x16_bf16 v[2:17], v[54:57], v[154:157], v[2:17]
	v_mul_f32_e32 v28, v28, v31
	v_mul_f32_e32 v30, v32, v66
	v_fmac_f32_e32 v20, v19, v201
	v_fmac_f32_e32 v24, v18, v200
	v_fmac_f32_e32 v28, v22, v199
	v_fmac_f32_e32 v30, v23, v198
	v_mfma_f32_32x32x16_bf16 v[2:17], v[50:53], v[142:145], v[2:17]
	v_add_f32_e32 v18, 1.0, v21
	v_exp_f32_e32 v19, v20
	v_add_f32_e32 v20, 1.0, v25
	v_exp_f32_e32 v21, v24
	v_exp_f32_e32 v22, v28
	v_exp_f32_e32 v23, v30
	v_mfma_f32_32x32x16_bf16 v[2:17], v[46:49], v[130:133], v[2:17]
	v_add_f32_e32 v24, 1.0, v26
	v_add_f32_e32 v25, 1.0, v29
	v_fmac_f32_e32 v18, v18, v19
	v_fmac_f32_e32 v20, v20, v21
	v_fmac_f32_e32 v24, v24, v22
	v_fmac_f32_e32 v25, v25, v23
	v_mfma_f32_32x32x16_bf16 v[2:17], v[42:45], v[134:137], v[2:17]
	v_rcp_f32_e32 v18, v18
	v_rcp_f32_e32 v20, v20
	v_rcp_f32_e32 v24, v24
	v_rcp_f32_e32 v25, v25
	v_mfma_f32_32x32x16_bf16 v[2:17], v[38:41], v[138:141], v[2:17]
	v_fma_f32 v18, -v19, v18, v18
	v_fma_f32 v19, -v21, v20, v20
	v_fma_f32 v20, -v22, v24, v24
	v_fma_f32 v21, -v23, v25, v25
	v_mfma_f32_32x32x16_bf16 v[2:17], v[34:37], v[146:149], v[2:17]
	v_cvt_pk_bf16_f32 v18, v18, v19
	v_cvt_pk_bf16_f32 v19, v20, v21
	ds_write_b64 v211, v[18:19] offset:8192
	s_nop 9
	v_exp_f32_e32 v4, v4
	v_exp_f32_e32 v8, v8
	v_exp_f32_e32 v12, v12
	v_exp_f32_e32 v16, v16
	v_exp_f32_e32 v2, v2
	v_add_f32_e32 v18, 1.0, v4
	v_exp_f32_e32 v6, v6
	v_exp_f32_e32 v10, v10
	v_exp_f32_e32 v14, v14
	v_add_f32_e32 v19, 1.0, v8
	v_add_f32_e32 v20, 1.0, v12
	v_add_f32_e32 v21, 1.0, v16
	v_exp_f32_e32 v3, v3
	v_fmac_f32_e32 v18, v2, v18
	v_exp_f32_e32 v2, v7
	v_exp_f32_e32 v7, v11
	v_exp_f32_e32 v11, v15
	v_fmac_f32_e32 v19, v6, v19
	v_fmac_f32_e32 v20, v10, v20
	v_fmac_f32_e32 v21, v14, v21
	v_add_f32_e32 v3, 1.0, v3
	v_rcp_f32_e32 v6, v18
	v_rcp_f32_e32 v10, v19
	v_rcp_f32_e32 v14, v20
	v_rcp_f32_e32 v15, v21
	v_fmamk_f32 v4, v4, 0x4038aa3b, v27
	v_add_f32_e32 v2, 1.0, v2
	v_fmamk_f32 v8, v8, 0x4038aa3b, v27
	v_add_f32_e32 v7, 1.0, v7
	v_rcp_f32_e32 v3, v3
	v_rcp_f32_e32 v2, v2
	v_exp_f32_e32 v5, v5
	v_exp_f32_e32 v9, v9
	v_fmamk_f32 v12, v12, 0x4038aa3b, v27
	v_add_f32_e32 v11, 1.0, v11
	v_fmac_f32_e32 v27, 0x4038aa3b, v16
	v_mul_f32_e32 v4, v4, v6
	v_rcp_f32_e32 v6, v7
	v_rcp_f32_e32 v7, v11
	v_exp_f32_e32 v11, v13
	v_exp_f32_e32 v13, v17
	v_mul_f32_e32 v8, v8, v10
	v_mul_f32_e32 v10, v12, v14
	v_mul_f32_e32 v12, v27, v15
	v_fmac_f32_e32 v4, v3, v207
	v_fmac_f32_e32 v8, v2, v206
	v_fmac_f32_e32 v10, v6, v209
	v_fmac_f32_e32 v12, v7, v208
	v_add_f32_e32 v2, 1.0, v5
	v_exp_f32_e32 v3, v4
	v_exp_f32_e32 v4, v8
	v_exp_f32_e32 v5, v10
	v_exp_f32_e32 v6, v12
	v_add_f32_e32 v7, 1.0, v9
	v_add_f32_e32 v8, 1.0, v11
	v_add_f32_e32 v9, 1.0, v13
	v_fmac_f32_e32 v2, v2, v3
	v_fmac_f32_e32 v7, v7, v4
	v_fmac_f32_e32 v8, v8, v5
	v_fmac_f32_e32 v9, v9, v6
	v_rcp_f32_e32 v2, v2
	v_rcp_f32_e32 v7, v7
	v_rcp_f32_e32 v8, v8
	v_rcp_f32_e32 v9, v9
	v_fma_f32 v2, -v3, v2, v2
	v_fma_f32 v3, -v4, v7, v7
	v_fma_f32 v4, -v5, v8, v8
	v_fma_f32 v5, -v6, v9, v9
	v_cvt_pk_bf16_f32 v2, v2, v3
	v_cvt_pk_bf16_f32 v3, v4, v5
	ds_write_b64 v211, v[2:3] offset:8200
	s_waitcnt lgkmcnt(0)
	s_barrier

.Llight_path:
	s_waitcnt vmcnt(0)
	v_mul_u32_u24_e32 v236, 36, v228
	v_add_u32_e32 v236, v236, v230
	v_add_u32_e32 v237, s7, v229
	v_mul_u32_u24_e32 v238, 0x104, v228
	v_add_u32_e32 v238, v238, v237
	v_add_u32_e32 v238, 0xb840, v238
	ds_read_b128 v[2:5], v237 offset:36928
	ds_read_b128 v[6:9], v237 offset:36944
	ds_read_b128 v[10:13], v237 offset:36960
	ds_read_b128 v[14:17], v237 offset:36976
	ds_read_b128 v[18:21], v237 offset:37056
	ds_read_b128 v[22:25], v237 offset:37072
	ds_read_b128 v[26:29], v237 offset:37088
	ds_read_b128 v[30:33], v237 offset:37104
	ds_read_b128 v[162:165], v236 offset:16384
	ds_read_b128 v[166:169], v236 offset:16416
	ds_read_b128 v[170:173], v236 offset:16448
	ds_read_b128 v[174:177], v236 offset:16480
	ds_read_b128 v[130:133], v237 offset:36928
	ds_read_b128 v[134:137], v237 offset:36944
	ds_read_b128 v[138:141], v237 offset:36960
	ds_read_b128 v[142:145], v237 offset:36976
	ds_read_b128 v[146:149], v237 offset:37056
	ds_read_b128 v[150:153], v237 offset:37072
	ds_read_b128 v[154:157], v237 offset:37088
	ds_read_b128 v[158:161], v237 offset:37104
	ds_read_b128 v[178:181], v236 offset:20992
	ds_read_b128 v[182:185], v236 offset:21024
	ds_read_b128 v[186:189], v236 offset:21056
	ds_read_b128 v[190:193], v236 offset:21088
	s_waitcnt lgkmcnt(12)
	v_mfma_f32_32x32x16_bf16 v[2:17], v[94:97], v[162:165], v[2:17]
	v_mfma_f32_32x32x16_bf16 v[2:17], v[90:93], v[166:169], v[2:17]
	v_mfma_f32_32x32x16_bf16 v[2:17], v[86:89], v[170:173], v[2:17]
	v_mfma_f32_32x32x16_bf16 v[2:17], v[82:85], v[174:177], v[2:17]
	v_mfma_f32_32x32x16_bf16 v[18:33], v[46:49], v[162:165], v[18:33]
	v_mfma_f32_32x32x16_bf16 v[18:33], v[42:45], v[166:169], v[18:33]
	v_mfma_f32_32x32x16_bf16 v[18:33], v[38:41], v[170:173], v[18:33]
	v_mfma_f32_32x32x16_bf16 v[18:33], v[34:37], v[174:177], v[18:33]
	s_waitcnt lgkmcnt(0)
	v_mfma_f32_32x32x16_bf16 v[130:145], v[94:97], v[178:181], v[130:145]
	v_mfma_f32_32x32x16_bf16 v[130:145], v[90:93], v[182:185], v[130:145]
	v_mfma_f32_32x32x16_bf16 v[130:145], v[86:89], v[186:189], v[130:145]
	v_mfma_f32_32x32x16_bf16 v[130:145], v[82:85], v[190:193], v[130:145]
	v_mfma_f32_32x32x16_bf16 v[146:161], v[46:49], v[178:181], v[146:161]
	v_mfma_f32_32x32x16_bf16 v[146:161], v[42:45], v[182:185], v[146:161]
	v_mfma_f32_32x32x16_bf16 v[146:161], v[38:41], v[186:189], v[146:161]
	v_mfma_f32_32x32x16_bf16 v[146:161], v[34:37], v[190:193], v[146:161]
	s_nop 7
	ds_write_b128 v238, v[2:5] offset:0
	ds_write_b128 v238, v[6:9] offset:16
	ds_write_b128 v238, v[10:13] offset:32
	ds_write_b128 v238, v[14:17] offset:48
	ds_write_b128 v238, v[18:21] offset:128
	ds_write_b128 v238, v[22:25] offset:144
	ds_write_b128 v238, v[26:29] offset:160
	ds_write_b128 v238, v[30:33] offset:176
	s_nop 7
	s_nop 7
	v_add_u32_e32 v239, 0x8200, v238
	ds_write_b128 v239, v[130:133] offset:0
	ds_write_b128 v239, v[134:137] offset:16
	ds_write_b128 v239, v[138:141] offset:32
	ds_write_b128 v239, v[142:145] offset:48
	v_add_u32_e32 v239, 0x8200, v238
	ds_write_b128 v239, v[146:149] offset:128
	ds_write_b128 v239, v[150:153] offset:144
	ds_write_b128 v239, v[154:157] offset:160
	ds_write_b128 v239, v[158:161] offset:176
	s_waitcnt lgkmcnt(0)
	ds_read_b128 v[2:5], v237 offset:36928
	ds_read_b128 v[6:9], v237 offset:36944
	ds_read_b128 v[10:13], v237 offset:36960
	ds_read_b128 v[14:17], v237 offset:36976
	ds_read_b128 v[18:21], v237 offset:37056
	ds_read_b128 v[22:25], v237 offset:37072
	ds_read_b128 v[26:29], v237 offset:37088
	ds_read_b128 v[30:33], v237 offset:37104
	ds_read_b128 v[162:165], v236 offset:25600
	ds_read_b128 v[166:169], v236 offset:25632
	ds_read_b128 v[170:173], v236 offset:25664
	ds_read_b128 v[174:177], v236 offset:25696
	ds_read_b128 v[130:133], v237 offset:36928
	ds_read_b128 v[134:137], v237 offset:36944
	ds_read_b128 v[138:141], v237 offset:36960
	ds_read_b128 v[142:145], v237 offset:36976
	ds_read_b128 v[146:149], v237 offset:37056
	ds_read_b128 v[150:153], v237 offset:37072
	ds_read_b128 v[154:157], v237 offset:37088
	ds_read_b128 v[158:161], v237 offset:37104
	ds_read_b128 v[178:181], v236 offset:30208
	ds_read_b128 v[182:185], v236 offset:30240
	ds_read_b128 v[186:189], v236 offset:30272
	ds_read_b128 v[190:193], v236 offset:30304
	s_waitcnt lgkmcnt(12)
	v_mfma_f32_32x32x16_bf16 v[2:17], v[94:97], v[162:165], v[2:17]
	v_mfma_f32_32x32x16_bf16 v[2:17], v[90:93], v[166:169], v[2:17]
	v_mfma_f32_32x32x16_bf16 v[2:17], v[86:89], v[170:173], v[2:17]
	v_mfma_f32_32x32x16_bf16 v[2:17], v[82:85], v[174:177], v[2:17]
	v_mfma_f32_32x32x16_bf16 v[18:33], v[46:49], v[162:165], v[18:33]
	v_mfma_f32_32x32x16_bf16 v[18:33], v[42:45], v[166:169], v[18:33]
	v_mfma_f32_32x32x16_bf16 v[18:33], v[38:41], v[170:173], v[18:33]
	v_mfma_f32_32x32x16_bf16 v[18:33], v[34:37], v[174:177], v[18:33]
	s_waitcnt lgkmcnt(0)
	v_mfma_f32_32x32x16_bf16 v[130:145], v[94:97], v[178:181], v[130:145]
	v_mfma_f32_32x32x16_bf16 v[130:145], v[90:93], v[182:185], v[130:145]
	v_mfma_f32_32x32x16_bf16 v[130:145], v[86:89], v[186:189], v[130:145]
	v_mfma_f32_32x32x16_bf16 v[130:145], v[82:85], v[190:193], v[130:145]
	v_mfma_f32_32x32x16_bf16 v[146:161], v[46:49], v[178:181], v[146:161]
	v_mfma_f32_32x32x16_bf16 v[146:161], v[42:45], v[182:185], v[146:161]
	v_mfma_f32_32x32x16_bf16 v[146:161], v[38:41], v[186:189], v[146:161]
	v_mfma_f32_32x32x16_bf16 v[146:161], v[34:37], v[190:193], v[146:161]
	s_nop 7
	v_add_u32_e32 v239, 0x10400, v238
	ds_write_b128 v239, v[2:5] offset:0
	ds_write_b128 v239, v[6:9] offset:16
	ds_write_b128 v239, v[10:13] offset:32
	ds_write_b128 v239, v[14:17] offset:48
	v_add_u32_e32 v239, 0x10400, v238
	ds_write_b128 v239, v[18:21] offset:128
	ds_write_b128 v239, v[22:25] offset:144
	ds_write_b128 v239, v[26:29] offset:160
	ds_write_b128 v239, v[30:33] offset:176
	s_nop 7
	s_nop 7
	v_cmp_gt_u32_e32 vcc, 16, v228
	s_and_saveexec_b64 s[20:21], vcc
	v_add_u32_e32 v239, 0x18600, v238
	ds_write_b128 v239, v[130:133] offset:0
	ds_write_b128 v239, v[134:137] offset:16
	ds_write_b128 v239, v[138:141] offset:32
	ds_write_b128 v239, v[142:145] offset:48
	v_add_u32_e32 v239, 0x18600, v238
	ds_write_b128 v239, v[146:149] offset:128
	ds_write_b128 v239, v[150:153] offset:144
	ds_write_b128 v239, v[154:157] offset:160
	ds_write_b128 v239, v[158:161] offset:176
	s_or_b64 exec, exec, s[20:21]
	s_waitcnt lgkmcnt(0)
	s_nop 7
	s_nop 7
	v_add_u32_e32 v231, s7, v229
	v_add_u32_e32 v231, 0xb840, v231
	v_add_u32_e32 v211, s6, v210
	s_mov_b32 s12, 0x4038aa3b
	v_mov_b32_e32 v235, 0xc038aa3b
	s_nop 0
	s_load_dwordx8 s[4:11], s[0:1], 0x10
	s_waitcnt lgkmcnt(0)
	v_add_u32_e32 v232, 0x24e80, v228
	ds_read_b32 v244, v232
	ds_read_b32 v245, v232 offset:128
	ds_read_b128 v[130:133], v210 offset:0
	ds_read_b128 v[134:137], v210 offset:1024
	ds_read_b128 v[138:141], v210 offset:2048
	ds_read_b128 v[142:145], v210 offset:3072
	ds_read_b128 v[146:149], v210 offset:4096
	ds_read_b128 v[150:153], v210 offset:5120
	ds_read_b128 v[154:157], v210 offset:6144
	ds_read_b128 v[158:161], v210 offset:7168
	v_mov_b32_e32 v194, 0
	v_mov_b32_e32 v195, 0
	v_mov_b32_e32 v196, 0
	v_mov_b32_e32 v197, 0
	v_mov_b32_e32 v198, 0
	v_mov_b32_e32 v199, 0
	v_mov_b32_e32 v200, 0
	v_mov_b32_e32 v201, 0
	v_mov_b32_e32 v202, 0
	v_mov_b32_e32 v203, 0
	v_mov_b32_e32 v204, 0
	v_mov_b32_e32 v205, 0
	v_mov_b32_e32 v206, 0
	v_mov_b32_e32 v207, 0
	v_mov_b32_e32 v208, 0
	v_mov_b32_e32 v209, 0
	v_add_u32_e32 v232, 0x100, v232
	s_waitcnt lgkmcnt(8)
	v_add_u32_e32 v233, v231, v244
	v_add_u32_e32 v234, v231, v245
	ds_read_b128 v[2:5], v233 offset:0
	ds_read_b128 v[6:9], v233 offset:16
	ds_read_b128 v[10:13], v233 offset:32
	ds_read_b128 v[14:17], v233 offset:48
	ds_read_b128 v[18:21], v233 offset:128
	ds_read_b128 v[22:25], v233 offset:144
	ds_read_b128 v[26:29], v233 offset:160
	ds_read_b128 v[30:33], v233 offset:176
	ds_read_b128 v[34:37], v234 offset:0
	ds_read_b128 v[38:41], v234 offset:16
	ds_read_b128 v[42:45], v234 offset:32
	ds_read_b128 v[46:49], v234 offset:48
	s_movk_i32 s16, 18
	s_waitcnt lgkmcnt(0)
	ds_read_b128 v[82:85], v234 offset:128
	ds_read_b128 v[86:89], v234 offset:144
	ds_read_b128 v[90:93], v234 offset:160
	ds_read_b128 v[94:97], v234 offset:176
	ds_read_b32 v244, v232 offset:0
	v_exp_f32_e32 v212, v4
	v_exp_f32_e32 v213, v8
	v_exp_f32_e32 v214, v12
	v_exp_f32_e32 v215, v16
	v_exp_f32_e32 v216, v2
	v_exp_f32_e32 v217, v6
	v_exp_f32_e32 v218, v10
	v_exp_f32_e32 v219, v14
	v_add_f32_e32 v236, 1.0, v212
	v_add_f32_e32 v237, 1.0, v213
	v_add_f32_e32 v238, 1.0, v214
	v_add_f32_e32 v239, 1.0, v215
	v_fma_f32 v240, v212, s12, v235
	v_fma_f32 v241, v213, s12, v235
	v_fma_f32 v242, v214, s12, v235
	v_fma_f32 v243, v215, s12, v235
	v_fmac_f32_e32 v236, v216, v236
	v_fmac_f32_e32 v237, v217, v237
	v_fmac_f32_e32 v238, v218, v238
	v_fmac_f32_e32 v239, v219, v239
	v_rcp_f32_e32 v216, v236
	v_rcp_f32_e32 v217, v237
	v_rcp_f32_e32 v218, v238
	v_rcp_f32_e32 v219, v239
	v_exp_f32_e32 v224, v5
	v_exp_f32_e32 v225, v9
	v_exp_f32_e32 v226, v13
	v_exp_f32_e32 v227, v17
	v_mul_f32_e32 v194, v240, v216
	v_mul_f32_e32 v195, v241, v217
	v_mul_f32_e32 v196, v242, v218
	v_mul_f32_e32 v197, v243, v219
	v_exp_f32_e32 v212, v194
	v_exp_f32_e32 v213, v195
	v_exp_f32_e32 v214, v196
	v_exp_f32_e32 v215, v197
	v_add_f32_e32 v224, 1.0, v224
	v_add_f32_e32 v225, 1.0, v225
	v_add_f32_e32 v226, 1.0, v226
	v_add_f32_e32 v227, 1.0, v227
	v_fmac_f32_e32 v224, v224, v212
	v_fmac_f32_e32 v225, v225, v213
	v_fmac_f32_e32 v226, v226, v214
	v_fmac_f32_e32 v227, v227, v215
	v_rcp_f32_e32 v224, v224
	v_rcp_f32_e32 v225, v225
	v_rcp_f32_e32 v226, v226
	v_rcp_f32_e32 v227, v227
	v_fma_f32 v224, -v212, v224, v224
	v_fma_f32 v225, -v213, v225, v225
	v_fma_f32 v226, -v214, v226, v226
	v_fma_f32 v227, -v215, v227, v227
	v_cvt_pk_bf16_f32 v224, v224, v225
	v_cvt_pk_bf16_f32 v225, v226, v227
	ds_write_b64 v211, v[224:225] offset:0
	s_waitcnt lgkmcnt(1)
	v_add_u32_e32 v233, v231, v244
	ds_read_b128 v[2:5], v233 offset:0
	ds_read_b128 v[6:9], v233 offset:16
	ds_read_b128 v[10:13], v233 offset:32
	ds_read_b128 v[14:17], v233 offset:48
	v_exp_f32_e32 v212, v20
	v_exp_f32_e32 v213, v24
	v_exp_f32_e32 v214, v28
	v_exp_f32_e32 v215, v32
	v_exp_f32_e32 v216, v18
	v_exp_f32_e32 v217, v22
	v_exp_f32_e32 v218, v26
	v_exp_f32_e32 v219, v30
	v_add_f32_e32 v236, 1.0, v212
	v_add_f32_e32 v237, 1.0, v213
	v_add_f32_e32 v238, 1.0, v214
	v_add_f32_e32 v239, 1.0, v215
	v_fma_f32 v240, v212, s12, v235
	v_fma_f32 v241, v213, s12, v235
	v_fma_f32 v242, v214, s12, v235
	v_fma_f32 v243, v215, s12, v235
	v_fmac_f32_e32 v236, v216, v236
	v_fmac_f32_e32 v237, v217, v237
	v_fmac_f32_e32 v238, v218, v238
	v_fmac_f32_e32 v239, v219, v239
	v_rcp_f32_e32 v216, v236
	v_rcp_f32_e32 v217, v237
	v_rcp_f32_e32 v218, v238
	v_rcp_f32_e32 v219, v239
	v_exp_f32_e32 v224, v21
	v_exp_f32_e32 v225, v25
	v_exp_f32_e32 v226, v29
	v_exp_f32_e32 v227, v33
	v_mul_f32_e32 v198, v240, v216
	v_mul_f32_e32 v199, v241, v217
	v_mul_f32_e32 v200, v242, v218
	v_mul_f32_e32 v201, v243, v219
	v_exp_f32_e32 v212, v198
	v_exp_f32_e32 v213, v199
	v_exp_f32_e32 v214, v200
	v_exp_f32_e32 v215, v201
	v_add_f32_e32 v224, 1.0, v224
	v_add_f32_e32 v225, 1.0, v225
	v_add_f32_e32 v226, 1.0, v226
	v_add_f32_e32 v227, 1.0, v227
	v_fmac_f32_e32 v224, v224, v212
	v_fmac_f32_e32 v225, v225, v213
	v_fmac_f32_e32 v226, v226, v214
	v_fmac_f32_e32 v227, v227, v215
	v_rcp_f32_e32 v224, v224
	v_rcp_f32_e32 v225, v225
	v_rcp_f32_e32 v226, v226
	v_rcp_f32_e32 v227, v227
	v_fma_f32 v224, -v212, v224, v224
	v_fma_f32 v225, -v213, v225, v225
	v_fma_f32 v226, -v214, v226, v226
	v_fma_f32 v227, -v215, v227, v227
	v_cvt_pk_bf16_f32 v224, v224, v225
	v_cvt_pk_bf16_f32 v225, v226, v227
	ds_write_b64 v211, v[224:225] offset:8
	s_waitcnt lgkmcnt(0)
	s_barrier
	ds_read_b128 v[130:133], v210 offset:0
	ds_read_b128 v[134:137], v210 offset:1024
	ds_read_b128 v[18:21], v233 offset:128
	ds_read_b128 v[22:25], v233 offset:144
	ds_read_b128 v[26:29], v233 offset:160
	ds_read_b128 v[30:33], v233 offset:176
	ds_read_b32 v245, v232 offset:128
	v_exp_f32_e32 v212, v36
	v_exp_f32_e32 v213, v40
	v_exp_f32_e32 v214, v44
	v_exp_f32_e32 v215, v48
	ds_read_b128 v[138:141], v210 offset:2048
	ds_read_b128 v[142:145], v210 offset:3072
	v_exp_f32_e32 v216, v34
	v_exp_f32_e32 v217, v38
	v_exp_f32_e32 v218, v42
	v_exp_f32_e32 v219, v46
	v_add_f32_e32 v236, 1.0, v212
	v_add_f32_e32 v237, 1.0, v213
	v_add_f32_e32 v238, 1.0, v214
	v_add_f32_e32 v239, 1.0, v215
	v_fma_f32 v240, v212, s12, v235
	v_fma_f32 v241, v213, s12, v235
	v_fma_f32 v242, v214, s12, v235
	v_fma_f32 v243, v215, s12, v235
	ds_read_b128 v[146:149], v210 offset:4096
	ds_read_b128 v[150:153], v210 offset:5120
	v_fmac_f32_e32 v236, v216, v236
	v_fmac_f32_e32 v237, v217, v237
	v_fmac_f32_e32 v238, v218, v238
	v_fmac_f32_e32 v239, v219, v239
	ds_read_b128 v[154:157], v210 offset:6144
	ds_read_b128 v[158:161], v210 offset:7168
	v_rcp_f32_e32 v216, v236
	v_rcp_f32_e32 v217, v237
	v_rcp_f32_e32 v218, v238
	v_rcp_f32_e32 v219, v239
	v_exp_f32_e32 v224, v37
	v_exp_f32_e32 v225, v41
	v_exp_f32_e32 v226, v45
	v_exp_f32_e32 v227, v49
	v_mul_f32_e32 v202, v240, v216
	v_mul_f32_e32 v203, v241, v217
	v_mul_f32_e32 v204, v242, v218
	v_mul_f32_e32 v205, v243, v219
	v_exp_f32_e32 v212, v202
	v_exp_f32_e32 v213, v203
	v_exp_f32_e32 v214, v204
	v_exp_f32_e32 v215, v205
	v_add_f32_e32 v224, 1.0, v224
	v_add_f32_e32 v225, 1.0, v225
	v_add_f32_e32 v226, 1.0, v226
	v_add_f32_e32 v227, 1.0, v227
	v_fmac_f32_e32 v224, v224, v212
	v_fmac_f32_e32 v225, v225, v213
	v_fmac_f32_e32 v226, v226, v214
	v_fmac_f32_e32 v227, v227, v215
	v_rcp_f32_e32 v224, v224
	v_rcp_f32_e32 v225, v225
	v_rcp_f32_e32 v226, v226
	v_rcp_f32_e32 v227, v227
	v_fma_f32 v224, -v212, v224, v224
	v_fma_f32 v225, -v213, v225, v225
	v_fma_f32 v226, -v214, v226, v226
	v_fma_f32 v227, -v215, v227, v227
	v_cvt_pk_bf16_f32 v224, v224, v225
	v_cvt_pk_bf16_f32 v225, v226, v227
	ds_write_b64 v211, v[224:225] offset:8192
	s_waitcnt lgkmcnt(1)
	v_mfma_f32_32x32x16_bf16 v[2:17], v[126:129], v[130:133], v[2:17]
	v_add_u32_e32 v234, v231, v245
	ds_read_b128 v[34:37], v234 offset:0
	ds_read_b128 v[38:41], v234 offset:16
	ds_read_b128 v[42:45], v234 offset:32
	ds_read_b128 v[46:49], v234 offset:48
	v_add_u32_e32 v232, 0x100, v232
	v_exp_f32_e32 v212, v84
	v_exp_f32_e32 v213, v88
	v_exp_f32_e32 v214, v92
	v_exp_f32_e32 v215, v96
	v_mfma_f32_32x32x16_bf16 v[2:17], v[122:125], v[134:137], v[2:17]
	v_exp_f32_e32 v216, v82
	v_exp_f32_e32 v217, v86
	v_exp_f32_e32 v218, v90
	v_exp_f32_e32 v219, v94
	v_add_f32_e32 v236, 1.0, v212
	v_add_f32_e32 v237, 1.0, v213
	v_add_f32_e32 v238, 1.0, v214
	v_add_f32_e32 v239, 1.0, v215
	v_fma_f32 v240, v212, s12, v235
	v_fma_f32 v241, v213, s12, v235
	v_fma_f32 v242, v214, s12, v235
	v_fma_f32 v243, v215, s12, v235
	v_mfma_f32_32x32x16_bf16 v[2:17], v[118:121], v[138:141], v[2:17]
	v_fmac_f32_e32 v236, v216, v236
	v_fmac_f32_e32 v237, v217, v237
	v_fmac_f32_e32 v238, v218, v238
	v_fmac_f32_e32 v239, v219, v239
	v_mfma_f32_32x32x16_bf16 v[2:17], v[114:117], v[142:145], v[2:17]
	v_rcp_f32_e32 v216, v236
	v_rcp_f32_e32 v217, v237
	v_rcp_f32_e32 v218, v238
	v_rcp_f32_e32 v219, v239
	v_mfma_f32_32x32x16_bf16 v[2:17], v[110:113], v[146:149], v[2:17]
	v_exp_f32_e32 v224, v85
	v_exp_f32_e32 v225, v89
	v_exp_f32_e32 v226, v93
	v_exp_f32_e32 v227, v97
	v_mul_f32_e32 v206, v240, v216
	v_mul_f32_e32 v207, v241, v217
	v_mul_f32_e32 v208, v242, v218
	v_mul_f32_e32 v209, v243, v219
	v_mfma_f32_32x32x16_bf16 v[2:17], v[106:109], v[150:153], v[2:17]
	v_mfma_f32_32x32x16_bf16 v[2:17], v[102:105], v[154:157], v[2:17]
	v_exp_f32_e32 v212, v206
	v_exp_f32_e32 v213, v207
	v_exp_f32_e32 v214, v208
	v_exp_f32_e32 v215, v209
	v_add_f32_e32 v224, 1.0, v224
	v_add_f32_e32 v225, 1.0, v225
	v_add_f32_e32 v226, 1.0, v226
	v_add_f32_e32 v227, 1.0, v227
	v_fmac_f32_e32 v224, v224, v212
	v_fmac_f32_e32 v225, v225, v213
	v_fmac_f32_e32 v226, v226, v214
	v_fmac_f32_e32 v227, v227, v215
	v_mfma_f32_32x32x16_bf16 v[2:17], v[98:101], v[158:161], v[2:17]
	v_rcp_f32_e32 v224, v224
	v_rcp_f32_e32 v225, v225
	v_rcp_f32_e32 v226, v226
	v_rcp_f32_e32 v227, v227
	v_fma_f32 v224, -v212, v224, v224
	v_fma_f32 v225, -v213, v225, v225
	v_fma_f32 v226, -v214, v226, v226
	v_fma_f32 v227, -v215, v227, v227
	v_cvt_pk_bf16_f32 v224, v224, v225
	v_cvt_pk_bf16_f32 v225, v226, v227
	ds_write_b64 v211, v[224:225] offset:8200
	s_waitcnt lgkmcnt(0)
	s_barrier
.Llight_loop:
	v_mfma_f32_32x32x16_bf16 v[18:33], v[78:81], v[130:133], v[18:33]
	ds_read_b128 v[162:165], v210 offset:8192
	ds_read_b128 v[166:169], v210 offset:9216
	ds_read_b128 v[82:85], v234 offset:128
	ds_read_b128 v[86:89], v234 offset:144
	ds_read_b128 v[90:93], v234 offset:160
	ds_read_b128 v[94:97], v234 offset:176
	ds_read_b32 v244, v232 offset:0
	v_exp_f32_e32 v212, v4
	v_exp_f32_e32 v213, v8
	v_exp_f32_e32 v214, v12
	v_exp_f32_e32 v215, v16
	v_mfma_f32_32x32x16_bf16 v[18:33], v[74:77], v[134:137], v[18:33]
	ds_read_b128 v[170:173], v210 offset:10240
	ds_read_b128 v[174:177], v210 offset:11264
	v_exp_f32_e32 v216, v2
	v_exp_f32_e32 v217, v6
	v_exp_f32_e32 v218, v10
	v_exp_f32_e32 v219, v14
	v_add_f32_e32 v236, 1.0, v212
	v_add_f32_e32 v237, 1.0, v213
	v_add_f32_e32 v238, 1.0, v214
	v_add_f32_e32 v239, 1.0, v215
	v_fma_f32 v240, v212, s12, v235
	v_fma_f32 v241, v213, s12, v235
	v_fma_f32 v242, v214, s12, v235
	v_fma_f32 v243, v215, s12, v235
	v_mfma_f32_32x32x16_bf16 v[18:33], v[70:73], v[138:141], v[18:33]
	ds_read_b128 v[178:181], v210 offset:12288
	ds_read_b128 v[182:185], v210 offset:13312
	v_exp_f32_e32 v220, v3
	v_exp_f32_e32 v221, v7
	v_exp_f32_e32 v222, v11
	v_exp_f32_e32 v223, v15
	v_fmac_f32_e32 v236, v216, v236
	v_fmac_f32_e32 v237, v217, v237
	v_fmac_f32_e32 v238, v218, v238
	v_fmac_f32_e32 v239, v219, v239
	v_mfma_f32_32x32x16_bf16 v[18:33], v[66:69], v[142:145], v[18:33]
	ds_read_b128 v[186:189], v210 offset:14336
	ds_read_b128 v[190:193], v210 offset:15360
	v_rcp_f32_e32 v216, v236
	v_rcp_f32_e32 v217, v237
	v_rcp_f32_e32 v218, v238
	v_rcp_f32_e32 v219, v239
	v_add_f32_e32 v220, 1.0, v220
	v_add_f32_e32 v221, 1.0, v221
	v_add_f32_e32 v222, 1.0, v222
	v_add_f32_e32 v223, 1.0, v223
	v_mfma_f32_32x32x16_bf16 v[18:33], v[62:65], v[146:149], v[18:33]
	v_rcp_f32_e32 v220, v220
	v_rcp_f32_e32 v221, v221
	v_rcp_f32_e32 v222, v222
	v_rcp_f32_e32 v223, v223
	v_mul_f32_e32 v240, v240, v216
	v_mul_f32_e32 v241, v241, v217
	v_mul_f32_e32 v242, v242, v218
	v_mul_f32_e32 v243, v243, v219
	v_mfma_f32_32x32x16_bf16 v[18:33], v[58:61], v[150:153], v[18:33]
	v_exp_f32_e32 v224, v5
	v_exp_f32_e32 v225, v9
	v_exp_f32_e32 v226, v13
	v_exp_f32_e32 v227, v17
	v_fma_f32 v194, v220, v194, v240
	v_fma_f32 v195, v221, v195, v241
	v_fma_f32 v196, v222, v196, v242
	v_fma_f32 v197, v223, v197, v243
	v_mfma_f32_32x32x16_bf16 v[18:33], v[54:57], v[154:157], v[18:33]
	v_exp_f32_e32 v212, v194
	v_exp_f32_e32 v213, v195
	v_exp_f32_e32 v214, v196
	v_exp_f32_e32 v215, v197
	v_add_f32_e32 v224, 1.0, v224
	v_add_f32_e32 v225, 1.0, v225
	v_add_f32_e32 v226, 1.0, v226
	v_add_f32_e32 v227, 1.0, v227
	v_fmac_f32_e32 v224, v224, v212
	v_fmac_f32_e32 v225, v225, v213
	v_fmac_f32_e32 v226, v226, v214
	v_fmac_f32_e32 v227, v227, v215
	v_mfma_f32_32x32x16_bf16 v[18:33], v[50:53], v[158:161], v[18:33]
	v_rcp_f32_e32 v224, v224
	v_rcp_f32_e32 v225, v225
	v_rcp_f32_e32 v226, v226
	v_rcp_f32_e32 v227, v227
	v_fma_f32 v224, -v212, v224, v224
	v_fma_f32 v225, -v213, v225, v225
	v_fma_f32 v226, -v214, v226, v226
	v_fma_f32 v227, -v215, v227, v227
	v_cvt_pk_bf16_f32 v224, v224, v225
	v_cvt_pk_bf16_f32 v225, v226, v227
	ds_write_b64 v211, v[224:225] offset:0
	s_waitcnt lgkmcnt(1)
	v_mfma_f32_32x32x16_bf16 v[34:49], v[126:129], v[162:165], v[34:49]
	v_add_u32_e32 v233, v231, v244
	ds_read_b128 v[2:5], v233 offset:0
	ds_read_b128 v[6:9], v233 offset:16
	ds_read_b128 v[10:13], v233 offset:32
	ds_read_b128 v[14:17], v233 offset:48
	v_exp_f32_e32 v212, v20
	v_exp_f32_e32 v213, v24
	v_exp_f32_e32 v214, v28
	v_exp_f32_e32 v215, v32
	v_mfma_f32_32x32x16_bf16 v[34:49], v[122:125], v[166:169], v[34:49]
	v_exp_f32_e32 v216, v18
	v_exp_f32_e32 v217, v22
	v_exp_f32_e32 v218, v26
	v_exp_f32_e32 v219, v30
	v_add_f32_e32 v236, 1.0, v212
	v_add_f32_e32 v237, 1.0, v213
	v_add_f32_e32 v238, 1.0, v214
	v_add_f32_e32 v239, 1.0, v215
	v_fma_f32 v240, v212, s12, v235
	v_fma_f32 v241, v213, s12, v235
	v_fma_f32 v242, v214, s12, v235
	v_fma_f32 v243, v215, s12, v235
	v_mfma_f32_32x32x16_bf16 v[34:49], v[118:121], v[170:173], v[34:49]
	v_exp_f32_e32 v220, v19
	v_exp_f32_e32 v221, v23
	v_exp_f32_e32 v222, v27
	v_exp_f32_e32 v223, v31
	v_fmac_f32_e32 v236, v216, v236
	v_fmac_f32_e32 v237, v217, v237
	v_fmac_f32_e32 v238, v218, v238
	v_fmac_f32_e32 v239, v219, v239
	v_mfma_f32_32x32x16_bf16 v[34:49], v[114:117], v[174:177], v[34:49]
	v_rcp_f32_e32 v216, v236
	v_rcp_f32_e32 v217, v237
	v_rcp_f32_e32 v218, v238
	v_rcp_f32_e32 v219, v239
	v_add_f32_e32 v220, 1.0, v220
	v_add_f32_e32 v221, 1.0, v221
	v_add_f32_e32 v222, 1.0, v222
	v_add_f32_e32 v223, 1.0, v223
	v_mfma_f32_32x32x16_bf16 v[34:49], v[110:113], v[178:181], v[34:49]
	v_rcp_f32_e32 v220, v220
	v_rcp_f32_e32 v221, v221
	v_rcp_f32_e32 v222, v222
	v_rcp_f32_e32 v223, v223
	v_mul_f32_e32 v240, v240, v216
	v_mul_f32_e32 v241, v241, v217
	v_mul_f32_e32 v242, v242, v218
	v_mul_f32_e32 v243, v243, v219
	v_mfma_f32_32x32x16_bf16 v[34:49], v[106:109], v[182:185], v[34:49]
	v_exp_f32_e32 v224, v21
	v_exp_f32_e32 v225, v25
	v_exp_f32_e32 v226, v29
	v_exp_f32_e32 v227, v33
	v_fma_f32 v198, v220, v198, v240
	v_fma_f32 v199, v221, v199, v241
	v_fma_f32 v200, v222, v200, v242
	v_fma_f32 v201, v223, v201, v243
	v_mfma_f32_32x32x16_bf16 v[34:49], v[102:105], v[186:189], v[34:49]
	v_exp_f32_e32 v212, v198
	v_exp_f32_e32 v213, v199
	v_exp_f32_e32 v214, v200
	v_exp_f32_e32 v215, v201
	v_add_f32_e32 v224, 1.0, v224
	v_add_f32_e32 v225, 1.0, v225
	v_add_f32_e32 v226, 1.0, v226
	v_add_f32_e32 v227, 1.0, v227
	v_fmac_f32_e32 v224, v224, v212
	v_fmac_f32_e32 v225, v225, v213
	v_fmac_f32_e32 v226, v226, v214
	v_fmac_f32_e32 v227, v227, v215
	v_mfma_f32_32x32x16_bf16 v[34:49], v[98:101], v[190:193], v[34:49]
	v_rcp_f32_e32 v224, v224
	v_rcp_f32_e32 v225, v225
	v_rcp_f32_e32 v226, v226
	v_rcp_f32_e32 v227, v227
	v_fma_f32 v224, -v212, v224, v224
	v_fma_f32 v225, -v213, v225, v225
	v_fma_f32 v226, -v214, v226, v226
	v_fma_f32 v227, -v215, v227, v227
	v_cvt_pk_bf16_f32 v224, v224, v225
	v_cvt_pk_bf16_f32 v225, v226, v227
	ds_write_b64 v211, v[224:225] offset:8
	s_waitcnt lgkmcnt(0)
	s_barrier
	v_mfma_f32_32x32x16_bf16 v[82:97], v[78:81], v[162:165], v[82:97]
	ds_read_b128 v[130:133], v210 offset:0
	ds_read_b128 v[134:137], v210 offset:1024
	ds_read_b128 v[18:21], v233 offset:128
	ds_read_b128 v[22:25], v233 offset:144
	ds_read_b128 v[26:29], v233 offset:160
	ds_read_b128 v[30:33], v233 offset:176
	ds_read_b32 v245, v232 offset:128
	v_exp_f32_e32 v212, v36
	v_exp_f32_e32 v213, v40
	v_exp_f32_e32 v214, v44
	v_exp_f32_e32 v215, v48
	v_mfma_f32_32x32x16_bf16 v[82:97], v[74:77], v[166:169], v[82:97]
	ds_read_b128 v[138:141], v210 offset:2048
	ds_read_b128 v[142:145], v210 offset:3072
	v_exp_f32_e32 v216, v34
	v_exp_f32_e32 v217, v38
	v_exp_f32_e32 v218, v42
	v_exp_f32_e32 v219, v46
	v_add_f32_e32 v236, 1.0, v212
	v_add_f32_e32 v237, 1.0, v213
	v_add_f32_e32 v238, 1.0, v214
	v_add_f32_e32 v239, 1.0, v215
	v_fma_f32 v240, v212, s12, v235
	v_fma_f32 v241, v213, s12, v235
	v_fma_f32 v242, v214, s12, v235
	v_fma_f32 v243, v215, s12, v235
	v_mfma_f32_32x32x16_bf16 v[82:97], v[70:73], v[170:173], v[82:97]
	ds_read_b128 v[146:149], v210 offset:4096
	ds_read_b128 v[150:153], v210 offset:5120
	v_exp_f32_e32 v220, v35
	v_exp_f32_e32 v221, v39
	v_exp_f32_e32 v222, v43
	v_exp_f32_e32 v223, v47
	v_fmac_f32_e32 v236, v216, v236
	v_fmac_f32_e32 v237, v217, v237
	v_fmac_f32_e32 v238, v218, v238
	v_fmac_f32_e32 v239, v219, v239
	v_mfma_f32_32x32x16_bf16 v[82:97], v[66:69], v[174:177], v[82:97]
	ds_read_b128 v[154:157], v210 offset:6144
	ds_read_b128 v[158:161], v210 offset:7168
	v_rcp_f32_e32 v216, v236
	v_rcp_f32_e32 v217, v237
	v_rcp_f32_e32 v218, v238
	v_rcp_f32_e32 v219, v239
	v_add_f32_e32 v220, 1.0, v220
	v_add_f32_e32 v221, 1.0, v221
	v_add_f32_e32 v222, 1.0, v222
	v_add_f32_e32 v223, 1.0, v223
	v_mfma_f32_32x32x16_bf16 v[82:97], v[62:65], v[178:181], v[82:97]
	v_rcp_f32_e32 v220, v220
	v_rcp_f32_e32 v221, v221
	v_rcp_f32_e32 v222, v222
	v_rcp_f32_e32 v223, v223
	v_mul_f32_e32 v240, v240, v216
	v_mul_f32_e32 v241, v241, v217
	v_mul_f32_e32 v242, v242, v218
	v_mul_f32_e32 v243, v243, v219
	v_mfma_f32_32x32x16_bf16 v[82:97], v[58:61], v[182:185], v[82:97]
	v_exp_f32_e32 v224, v37
	v_exp_f32_e32 v225, v41
	v_exp_f32_e32 v226, v45
	v_exp_f32_e32 v227, v49
	v_fma_f32 v202, v220, v202, v240
	v_fma_f32 v203, v221, v203, v241
	v_fma_f32 v204, v222, v204, v242
	v_fma_f32 v205, v223, v205, v243
	v_mfma_f32_32x32x16_bf16 v[82:97], v[54:57], v[186:189], v[82:97]
	v_exp_f32_e32 v212, v202
	v_exp_f32_e32 v213, v203
	v_exp_f32_e32 v214, v204
	v_exp_f32_e32 v215, v205
	v_add_f32_e32 v224, 1.0, v224
	v_add_f32_e32 v225, 1.0, v225
	v_add_f32_e32 v226, 1.0, v226
	v_add_f32_e32 v227, 1.0, v227
	v_fmac_f32_e32 v224, v224, v212
	v_fmac_f32_e32 v225, v225, v213
	v_fmac_f32_e32 v226, v226, v214
	v_fmac_f32_e32 v227, v227, v215
	v_mfma_f32_32x32x16_bf16 v[82:97], v[50:53], v[190:193], v[82:97]
	v_rcp_f32_e32 v224, v224
	v_rcp_f32_e32 v225, v225
	v_rcp_f32_e32 v226, v226
	v_rcp_f32_e32 v227, v227
	v_fma_f32 v224, -v212, v224, v224
	v_fma_f32 v225, -v213, v225, v225
	v_fma_f32 v226, -v214, v226, v226
	v_fma_f32 v227, -v215, v227, v227
	v_cvt_pk_bf16_f32 v224, v224, v225
	v_cvt_pk_bf16_f32 v225, v226, v227
	ds_write_b64 v211, v[224:225] offset:8192
	s_waitcnt lgkmcnt(1)
	v_mfma_f32_32x32x16_bf16 v[2:17], v[126:129], v[130:133], v[2:17]
	v_add_u32_e32 v234, v231, v245
	ds_read_b128 v[34:37], v234 offset:0
	ds_read_b128 v[38:41], v234 offset:16
	ds_read_b128 v[42:45], v234 offset:32
	ds_read_b128 v[46:49], v234 offset:48
	v_add_u32_e32 v232, 0x100, v232
	v_exp_f32_e32 v212, v84
	v_exp_f32_e32 v213, v88
	v_exp_f32_e32 v214, v92
	v_exp_f32_e32 v215, v96
	v_mfma_f32_32x32x16_bf16 v[2:17], v[122:125], v[134:137], v[2:17]
	v_exp_f32_e32 v216, v82
	v_exp_f32_e32 v217, v86
	v_exp_f32_e32 v218, v90
	v_exp_f32_e32 v219, v94
	v_add_f32_e32 v236, 1.0, v212
	v_add_f32_e32 v237, 1.0, v213
	v_add_f32_e32 v238, 1.0, v214
	v_add_f32_e32 v239, 1.0, v215
	v_fma_f32 v240, v212, s12, v235
	v_fma_f32 v241, v213, s12, v235
	v_fma_f32 v242, v214, s12, v235
	v_fma_f32 v243, v215, s12, v235
	v_mfma_f32_32x32x16_bf16 v[2:17], v[118:121], v[138:141], v[2:17]
	v_exp_f32_e32 v220, v83
	v_exp_f32_e32 v221, v87
	v_exp_f32_e32 v222, v91
	v_exp_f32_e32 v223, v95
	v_fmac_f32_e32 v236, v216, v236
	v_fmac_f32_e32 v237, v217, v237
	v_fmac_f32_e32 v238, v218, v238
	v_fmac_f32_e32 v239, v219, v239
	v_mfma_f32_32x32x16_bf16 v[2:17], v[114:117], v[142:145], v[2:17]
	v_rcp_f32_e32 v216, v236
	v_rcp_f32_e32 v217, v237
	v_rcp_f32_e32 v218, v238
	v_rcp_f32_e32 v219, v239
	v_add_f32_e32 v220, 1.0, v220
	v_add_f32_e32 v221, 1.0, v221
	v_add_f32_e32 v222, 1.0, v222
	v_add_f32_e32 v223, 1.0, v223
	v_mfma_f32_32x32x16_bf16 v[2:17], v[110:113], v[146:149], v[2:17]
	v_rcp_f32_e32 v220, v220
	v_rcp_f32_e32 v221, v221
	v_rcp_f32_e32 v222, v222
	v_rcp_f32_e32 v223, v223
	v_mul_f32_e32 v240, v240, v216
	v_mul_f32_e32 v241, v241, v217
	v_mul_f32_e32 v242, v242, v218
	v_mul_f32_e32 v243, v243, v219
	v_mfma_f32_32x32x16_bf16 v[2:17], v[106:109], v[150:153], v[2:17]
	v_exp_f32_e32 v224, v85
	v_exp_f32_e32 v225, v89
	v_exp_f32_e32 v226, v93
	v_exp_f32_e32 v227, v97
	v_fma_f32 v206, v220, v206, v240
	v_fma_f32 v207, v221, v207, v241
	v_fma_f32 v208, v222, v208, v242
	v_fma_f32 v209, v223, v209, v243
	v_mfma_f32_32x32x16_bf16 v[2:17], v[102:105], v[154:157], v[2:17]
	v_exp_f32_e32 v212, v206
	v_exp_f32_e32 v213, v207
	v_exp_f32_e32 v214, v208
	v_exp_f32_e32 v215, v209
	v_add_f32_e32 v224, 1.0, v224
	v_add_f32_e32 v225, 1.0, v225
	v_add_f32_e32 v226, 1.0, v226
	v_add_f32_e32 v227, 1.0, v227
	v_fmac_f32_e32 v224, v224, v212
	v_fmac_f32_e32 v225, v225, v213
	v_fmac_f32_e32 v226, v226, v214
	v_fmac_f32_e32 v227, v227, v215
	v_mfma_f32_32x32x16_bf16 v[2:17], v[98:101], v[158:161], v[2:17]
	v_rcp_f32_e32 v224, v224
	v_rcp_f32_e32 v225, v225
	v_rcp_f32_e32 v226, v226
	v_rcp_f32_e32 v227, v227
	v_fma_f32 v224, -v212, v224, v224
	v_fma_f32 v225, -v213, v225, v225
	v_fma_f32 v226, -v214, v226, v226
	v_fma_f32 v227, -v215, v227, v227
	v_cvt_pk_bf16_f32 v224, v224, v225
	v_cvt_pk_bf16_f32 v225, v226, v227
	ds_write_b64 v211, v[224:225] offset:8200
	s_waitcnt lgkmcnt(0)
	s_barrier
	s_sub_u32 s16, s16, 1
	s_cmp_lg_u32 s16, 0
	s_cbranch_scc1 .Llight_loop
	v_mfma_f32_32x32x16_bf16 v[18:33], v[78:81], v[130:133], v[18:33]
	ds_read_b128 v[162:165], v210 offset:8192
	ds_read_b128 v[166:169], v210 offset:9216
	ds_read_b128 v[82:85], v234 offset:128
	ds_read_b128 v[86:89], v234 offset:144
	ds_read_b128 v[90:93], v234 offset:160
	ds_read_b128 v[94:97], v234 offset:176
	v_exp_f32_e32 v212, v4
	v_exp_f32_e32 v213, v8
	v_exp_f32_e32 v214, v12
	v_exp_f32_e32 v215, v16
	v_mfma_f32_32x32x16_bf16 v[18:33], v[74:77], v[134:137], v[18:33]
	ds_read_b128 v[170:173], v210 offset:10240
	ds_read_b128 v[174:177], v210 offset:11264
	v_exp_f32_e32 v216, v2
	v_exp_f32_e32 v217, v6
	v_exp_f32_e32 v218, v10
	v_exp_f32_e32 v219, v14
	v_add_f32_e32 v236, 1.0, v212
	v_add_f32_e32 v237, 1.0, v213
	v_add_f32_e32 v238, 1.0, v214
	v_add_f32_e32 v239, 1.0, v215
	v_fma_f32 v240, v212, s12, v235
	v_fma_f32 v241, v213, s12, v235
	v_fma_f32 v242, v214, s12, v235
	v_fma_f32 v243, v215, s12, v235
	v_mfma_f32_32x32x16_bf16 v[18:33], v[70:73], v[138:141], v[18:33]
	ds_read_b128 v[178:181], v210 offset:12288
	ds_read_b128 v[182:185], v210 offset:13312
	v_exp_f32_e32 v220, v3
	v_exp_f32_e32 v221, v7
	v_exp_f32_e32 v222, v11
	v_exp_f32_e32 v223, v15
	v_fmac_f32_e32 v236, v216, v236
	v_fmac_f32_e32 v237, v217, v237
	v_fmac_f32_e32 v238, v218, v238
	v_fmac_f32_e32 v239, v219, v239
	v_mfma_f32_32x32x16_bf16 v[18:33], v[66:69], v[142:145], v[18:33]
	ds_read_b128 v[186:189], v210 offset:14336
	ds_read_b128 v[190:193], v210 offset:15360
	v_rcp_f32_e32 v216, v236
	v_rcp_f32_e32 v217, v237
	v_rcp_f32_e32 v218, v238
	v_rcp_f32_e32 v219, v239
	v_add_f32_e32 v220, 1.0, v220
	v_add_f32_e32 v221, 1.0, v221
	v_add_f32_e32 v222, 1.0, v222
	v_add_f32_e32 v223, 1.0, v223
	v_mfma_f32_32x32x16_bf16 v[18:33], v[62:65], v[146:149], v[18:33]
	v_rcp_f32_e32 v220, v220
	v_rcp_f32_e32 v221, v221
	v_rcp_f32_e32 v222, v222
	v_rcp_f32_e32 v223, v223
	v_mul_f32_e32 v240, v240, v216
	v_mul_f32_e32 v241, v241, v217
	v_mul_f32_e32 v242, v242, v218
	v_mul_f32_e32 v243, v243, v219
	v_mfma_f32_32x32x16_bf16 v[18:33], v[58:61], v[150:153], v[18:33]
	v_exp_f32_e32 v224, v5
	v_exp_f32_e32 v225, v9
	v_exp_f32_e32 v226, v13
	v_exp_f32_e32 v227, v17
	v_fma_f32 v194, v220, v194, v240
	v_fma_f32 v195, v221, v195, v241
	v_fma_f32 v196, v222, v196, v242
	v_fma_f32 v197, v223, v197, v243
	v_mfma_f32_32x32x16_bf16 v[18:33], v[54:57], v[154:157], v[18:33]
	v_exp_f32_e32 v212, v194
	v_exp_f32_e32 v213, v195
	v_exp_f32_e32 v214, v196
	v_exp_f32_e32 v215, v197
	v_add_f32_e32 v224, 1.0, v224
	v_add_f32_e32 v225, 1.0, v225
	v_add_f32_e32 v226, 1.0, v226
	v_add_f32_e32 v227, 1.0, v227
	v_fmac_f32_e32 v224, v224, v212
	v_fmac_f32_e32 v225, v225, v213
	v_fmac_f32_e32 v226, v226, v214
	v_fmac_f32_e32 v227, v227, v215
	v_mfma_f32_32x32x16_bf16 v[18:33], v[50:53], v[158:161], v[18:33]
	v_rcp_f32_e32 v224, v224
	v_rcp_f32_e32 v225, v225
	v_rcp_f32_e32 v226, v226
	v_rcp_f32_e32 v227, v227
	v_fma_f32 v224, -v212, v224, v224
	v_fma_f32 v225, -v213, v225, v225
	v_fma_f32 v226, -v214, v226, v226
	v_fma_f32 v227, -v215, v227, v227
	v_cvt_pk_bf16_f32 v224, v224, v225
	v_cvt_pk_bf16_f32 v225, v226, v227
	ds_write_b64 v211, v[224:225] offset:0
	s_waitcnt lgkmcnt(1)
	v_mfma_f32_32x32x16_bf16 v[34:49], v[126:129], v[162:165], v[34:49]
	v_exp_f32_e32 v212, v20
	v_exp_f32_e32 v213, v24
	v_exp_f32_e32 v214, v28
	v_exp_f32_e32 v215, v32
	v_mfma_f32_32x32x16_bf16 v[34:49], v[122:125], v[166:169], v[34:49]
	v_exp_f32_e32 v216, v18
	v_exp_f32_e32 v217, v22
	v_exp_f32_e32 v218, v26
	v_exp_f32_e32 v219, v30
	v_add_f32_e32 v236, 1.0, v212
	v_add_f32_e32 v237, 1.0, v213
	v_add_f32_e32 v238, 1.0, v214
	v_add_f32_e32 v239, 1.0, v215
	v_fma_f32 v240, v212, s12, v235
	v_fma_f32 v241, v213, s12, v235
	v_fma_f32 v242, v214, s12, v235
	v_fma_f32 v243, v215, s12, v235
	v_mfma_f32_32x32x16_bf16 v[34:49], v[118:121], v[170:173], v[34:49]
	v_exp_f32_e32 v220, v19
	v_exp_f32_e32 v221, v23
	v_exp_f32_e32 v222, v27
	v_exp_f32_e32 v223, v31
	v_fmac_f32_e32 v236, v216, v236
	v_fmac_f32_e32 v237, v217, v237
	v_fmac_f32_e32 v238, v218, v238
	v_fmac_f32_e32 v239, v219, v239
	v_mfma_f32_32x32x16_bf16 v[34:49], v[114:117], v[174:177], v[34:49]
	v_rcp_f32_e32 v216, v236
	v_rcp_f32_e32 v217, v237
	v_rcp_f32_e32 v218, v238
	v_rcp_f32_e32 v219, v239
	v_add_f32_e32 v220, 1.0, v220
	v_add_f32_e32 v221, 1.0, v221
	v_add_f32_e32 v222, 1.0, v222
	v_add_f32_e32 v223, 1.0, v223
	v_mfma_f32_32x32x16_bf16 v[34:49], v[110:113], v[178:181], v[34:49]
	v_rcp_f32_e32 v220, v220
	v_rcp_f32_e32 v221, v221
	v_rcp_f32_e32 v222, v222
	v_rcp_f32_e32 v223, v223
	v_mul_f32_e32 v240, v240, v216
	v_mul_f32_e32 v241, v241, v217
	v_mul_f32_e32 v242, v242, v218
	v_mul_f32_e32 v243, v243, v219
	v_mfma_f32_32x32x16_bf16 v[34:49], v[106:109], v[182:185], v[34:49]
	v_exp_f32_e32 v224, v21
	v_exp_f32_e32 v225, v25
	v_exp_f32_e32 v226, v29
	v_exp_f32_e32 v227, v33
	v_fma_f32 v198, v220, v198, v240
	v_fma_f32 v199, v221, v199, v241
	v_fma_f32 v200, v222, v200, v242
	v_fma_f32 v201, v223, v201, v243
	v_mfma_f32_32x32x16_bf16 v[34:49], v[102:105], v[186:189], v[34:49]
	v_exp_f32_e32 v212, v198
	v_exp_f32_e32 v213, v199
	v_exp_f32_e32 v214, v200
	v_exp_f32_e32 v215, v201
	v_add_f32_e32 v224, 1.0, v224
	v_add_f32_e32 v225, 1.0, v225
	v_add_f32_e32 v226, 1.0, v226
	v_add_f32_e32 v227, 1.0, v227
	v_fmac_f32_e32 v224, v224, v212
	v_fmac_f32_e32 v225, v225, v213
	v_fmac_f32_e32 v226, v226, v214
	v_fmac_f32_e32 v227, v227, v215
	v_mfma_f32_32x32x16_bf16 v[34:49], v[98:101], v[190:193], v[34:49]
	v_rcp_f32_e32 v224, v224
	v_rcp_f32_e32 v225, v225
	v_rcp_f32_e32 v226, v226
	v_rcp_f32_e32 v227, v227
	v_fma_f32 v224, -v212, v224, v224
	v_fma_f32 v225, -v213, v225, v225
	v_fma_f32 v226, -v214, v226, v226
	v_fma_f32 v227, -v215, v227, v227
	v_cvt_pk_bf16_f32 v224, v224, v225
	v_cvt_pk_bf16_f32 v225, v226, v227
	ds_write_b64 v211, v[224:225] offset:8
	s_waitcnt lgkmcnt(0)
	s_barrier
	v_mfma_f32_32x32x16_bf16 v[82:97], v[78:81], v[162:165], v[82:97]
	v_exp_f32_e32 v212, v36
	v_exp_f32_e32 v213, v40
	v_exp_f32_e32 v214, v44
	v_exp_f32_e32 v215, v48
	v_mfma_f32_32x32x16_bf16 v[82:97], v[74:77], v[166:169], v[82:97]
	v_exp_f32_e32 v216, v34
	v_exp_f32_e32 v217, v38
	v_exp_f32_e32 v218, v42
	v_exp_f32_e32 v219, v46
	v_add_f32_e32 v236, 1.0, v212
	v_add_f32_e32 v237, 1.0, v213
	v_add_f32_e32 v238, 1.0, v214
	v_add_f32_e32 v239, 1.0, v215
	v_fma_f32 v240, v212, s12, v235
	v_fma_f32 v241, v213, s12, v235
	v_fma_f32 v242, v214, s12, v235
	v_fma_f32 v243, v215, s12, v235
	v_mfma_f32_32x32x16_bf16 v[82:97], v[70:73], v[170:173], v[82:97]
	v_exp_f32_e32 v220, v35
	v_exp_f32_e32 v221, v39
	v_exp_f32_e32 v222, v43
	v_exp_f32_e32 v223, v47
	v_fmac_f32_e32 v236, v216, v236
	v_fmac_f32_e32 v237, v217, v237
	v_fmac_f32_e32 v238, v218, v238
	v_fmac_f32_e32 v239, v219, v239
	v_mfma_f32_32x32x16_bf16 v[82:97], v[66:69], v[174:177], v[82:97]
	v_rcp_f32_e32 v216, v236
	v_rcp_f32_e32 v217, v237
	v_rcp_f32_e32 v218, v238
	v_rcp_f32_e32 v219, v239
	v_add_f32_e32 v220, 1.0, v220
	v_add_f32_e32 v221, 1.0, v221
	v_add_f32_e32 v222, 1.0, v222
	v_add_f32_e32 v223, 1.0, v223
	v_mfma_f32_32x32x16_bf16 v[82:97], v[62:65], v[178:181], v[82:97]
	v_rcp_f32_e32 v220, v220
	v_rcp_f32_e32 v221, v221
	v_rcp_f32_e32 v222, v222
	v_rcp_f32_e32 v223, v223
	v_mul_f32_e32 v240, v240, v216
	v_mul_f32_e32 v241, v241, v217
	v_mul_f32_e32 v242, v242, v218
	v_mul_f32_e32 v243, v243, v219
	v_mfma_f32_32x32x16_bf16 v[82:97], v[58:61], v[182:185], v[82:97]
	v_exp_f32_e32 v224, v37
	v_exp_f32_e32 v225, v41
	v_exp_f32_e32 v226, v45
	v_exp_f32_e32 v227, v49
	v_fma_f32 v202, v220, v202, v240
	v_fma_f32 v203, v221, v203, v241
	v_fma_f32 v204, v222, v204, v242
	v_fma_f32 v205, v223, v205, v243
	v_mfma_f32_32x32x16_bf16 v[82:97], v[54:57], v[186:189], v[82:97]
	v_exp_f32_e32 v212, v202
	v_exp_f32_e32 v213, v203
	v_exp_f32_e32 v214, v204
	v_exp_f32_e32 v215, v205
	v_add_f32_e32 v224, 1.0, v224
	v_add_f32_e32 v225, 1.0, v225
	v_add_f32_e32 v226, 1.0, v226
	v_add_f32_e32 v227, 1.0, v227
	v_fmac_f32_e32 v224, v224, v212
	v_fmac_f32_e32 v225, v225, v213
	v_fmac_f32_e32 v226, v226, v214
	v_fmac_f32_e32 v227, v227, v215
	v_mfma_f32_32x32x16_bf16 v[82:97], v[50:53], v[190:193], v[82:97]
	v_rcp_f32_e32 v224, v224
	v_rcp_f32_e32 v225, v225
	v_rcp_f32_e32 v226, v226
	v_rcp_f32_e32 v227, v227
	v_fma_f32 v224, -v212, v224, v224
	v_fma_f32 v225, -v213, v225, v225
	v_fma_f32 v226, -v214, v226, v226
	v_fma_f32 v227, -v215, v227, v227
	v_cvt_pk_bf16_f32 v224, v224, v225
	v_cvt_pk_bf16_f32 v225, v226, v227
	ds_write_b64 v211, v[224:225] offset:8192
	s_waitcnt lgkmcnt(1)
	v_exp_f32_e32 v212, v84
	v_exp_f32_e32 v213, v88
	v_exp_f32_e32 v214, v92
	v_exp_f32_e32 v215, v96
	v_exp_f32_e32 v216, v82
	v_exp_f32_e32 v217, v86
	v_exp_f32_e32 v218, v90
	v_exp_f32_e32 v219, v94
	v_add_f32_e32 v236, 1.0, v212
	v_add_f32_e32 v237, 1.0, v213
	v_add_f32_e32 v238, 1.0, v214
	v_add_f32_e32 v239, 1.0, v215
	v_fma_f32 v240, v212, s12, v235
	v_fma_f32 v241, v213, s12, v235
	v_fma_f32 v242, v214, s12, v235
	v_fma_f32 v243, v215, s12, v235
	v_exp_f32_e32 v220, v83
	v_exp_f32_e32 v221, v87
	v_exp_f32_e32 v222, v91
	v_exp_f32_e32 v223, v95
	v_fmac_f32_e32 v236, v216, v236
	v_fmac_f32_e32 v237, v217, v237
	v_fmac_f32_e32 v238, v218, v238
	v_fmac_f32_e32 v239, v219, v239
	v_rcp_f32_e32 v216, v236
	v_rcp_f32_e32 v217, v237
	v_rcp_f32_e32 v218, v238
	v_rcp_f32_e32 v219, v239
	v_add_f32_e32 v220, 1.0, v220
	v_add_f32_e32 v221, 1.0, v221
	v_add_f32_e32 v222, 1.0, v222
	v_add_f32_e32 v223, 1.0, v223
	v_rcp_f32_e32 v220, v220
	v_rcp_f32_e32 v221, v221
	v_rcp_f32_e32 v222, v222
	v_rcp_f32_e32 v223, v223
	v_mul_f32_e32 v240, v240, v216
	v_mul_f32_e32 v241, v241, v217
	v_mul_f32_e32 v242, v242, v218
	v_mul_f32_e32 v243, v243, v219
	v_exp_f32_e32 v224, v85
	v_exp_f32_e32 v225, v89
	v_exp_f32_e32 v226, v93
	v_exp_f32_e32 v227, v97
	v_fma_f32 v206, v220, v206, v240
	v_fma_f32 v207, v221, v207, v241
	v_fma_f32 v208, v222, v208, v242
	v_fma_f32 v209, v223, v209, v243
	v_exp_f32_e32 v212, v206
	v_exp_f32_e32 v213, v207
	v_exp_f32_e32 v214, v208
	v_exp_f32_e32 v215, v209
	v_add_f32_e32 v224, 1.0, v224
	v_add_f32_e32 v225, 1.0, v225
	v_add_f32_e32 v226, 1.0, v226
	v_add_f32_e32 v227, 1.0, v227
	v_fmac_f32_e32 v224, v224, v212
	v_fmac_f32_e32 v225, v225, v213
	v_fmac_f32_e32 v226, v226, v214
	v_fmac_f32_e32 v227, v227, v215
	v_rcp_f32_e32 v224, v224
	v_rcp_f32_e32 v225, v225
	v_rcp_f32_e32 v226, v226
	v_rcp_f32_e32 v227, v227
	v_fma_f32 v224, -v212, v224, v224
	v_fma_f32 v225, -v213, v225, v225
	v_fma_f32 v226, -v214, v226, v226
	v_fma_f32 v227, -v215, v227, v227
	v_cvt_pk_bf16_f32 v224, v224, v225
	v_cvt_pk_bf16_f32 v225, v226, v227
	ds_write_b64 v211, v[224:225] offset:8200
	s_waitcnt lgkmcnt(0)
	s_barrier
	s_nop 7
	s_nop 7
	s_branch .Lepilogue
